# GEMM K-loops: duplicate post-barrier lgkmcnt wait dropped + loop-counter SALU rotated in front of the loop-back barrier (stacked segment-boundary trims)
# baseline (speedup 1.0000x reference)
.LBB0_180:
	ds_read_b128 v[170:173], v163
	ds_read_b128 v[174:177], v163 offset:1024
	ds_read_b128 v[178:181], v163 offset:2048
	ds_read_b128 v[182:185], v163 offset:3072
	ds_read_b128 v[186:189], v164
	ds_read_b128 v[190:193], v164 offset:1024
	ds_read_b128 v[194:197], v164 offset:2048
	ds_read_b128 v[198:201], v164 offset:3072
	s_add_u32 s54, s50, s4
	s_addc_u32 s55, s51, s5
	s_cmpk_eq_i32 s4, 0x1000
	s_cselect_b64 vcc, -1, 0
	s_and_b64 s[52:53], vcc, exec
	s_cselect_b32 s72, 0, s4
	s_cselect_b32 s71, 0, s5
	s_cselect_b32 s52, s47, s54
	s_cselect_b32 s53, s7, s55
	s_add_u32 s54, s18, s72
	v_cndmask_b32_e32 v140, v128, v166, vcc
	v_cndmask_b32_e32 v129, v132, v168, vcc
	v_cndmask_b32_e32 v154, v130, v167, vcc
	v_cndmask_b32_e32 v131, v134, v169, vcc
	s_addc_u32 s55, s19, s71
	v_lshl_add_u64 v[234:235], v[152:153], 0, s[4:5]
	v_lshl_add_u64 v[234:235], v[234:235], 0, s[14:15]
	s_add_i32 m0, s1, 0xc000
	ds_read_b128 v[202:205], v165
	ds_read_b128 v[206:209], v165 offset:1024
	ds_read_b128 v[210:213], v165 offset:2048
	ds_read_b128 v[214:217], v165 offset:3072
	ds_read_b128 v[218:221], v165 offset:4096
	ds_read_b128 v[222:225], v165 offset:5120
	ds_read_b128 v[226:229], v165 offset:6144
	ds_read_b128 v[230:233], v165 offset:7168
	global_load_lds_dwordx4 v[234:235], off
	v_lshl_add_u64 v[234:235], v[150:151], 0, s[4:5]
	v_lshl_add_u64 v[234:235], v[234:235], 0, s[14:15]
	s_add_i32 m0, s1, 0xe000
	s_nop 0
	global_load_lds_dwordx4 v[234:235], off
	s_waitcnt vmcnt(8)
	s_waitcnt lgkmcnt(0)
	s_barrier
	s_setprio 1
	v_mfma_f32_16x16x32_bf16 v[60:63], v[170:173], v[202:205], v[60:63]
	v_mfma_f32_16x16x32_bf16 v[56:59], v[178:181], v[202:205], v[56:59]
	v_mfma_f32_16x16x32_bf16 v[52:55], v[170:173], v[210:213], v[52:55]
	v_mfma_f32_16x16x32_bf16 v[48:51], v[178:181], v[210:213], v[48:51]
	v_mfma_f32_16x16x32_bf16 v[44:47], v[170:173], v[218:221], v[44:47]
	v_mfma_f32_16x16x32_bf16 v[40:43], v[178:181], v[218:221], v[40:43]
	v_mfma_f32_16x16x32_bf16 v[36:39], v[170:173], v[226:229], v[36:39]
	v_mfma_f32_16x16x32_bf16 v[32:35], v[178:181], v[226:229], v[32:35]
	v_mfma_f32_16x16x32_bf16 v[60:63], v[174:177], v[206:209], v[60:63]
	v_mfma_f32_16x16x32_bf16 v[56:59], v[182:185], v[206:209], v[56:59]
	v_mfma_f32_16x16x32_bf16 v[52:55], v[174:177], v[214:217], v[52:55]
	v_mfma_f32_16x16x32_bf16 v[48:51], v[182:185], v[214:217], v[48:51]
	v_mfma_f32_16x16x32_bf16 v[44:47], v[174:177], v[222:225], v[44:47]
	v_mfma_f32_16x16x32_bf16 v[40:43], v[182:185], v[222:225], v[40:43]
	v_mfma_f32_16x16x32_bf16 v[36:39], v[174:177], v[230:233], v[36:39]
	v_mfma_f32_16x16x32_bf16 v[32:35], v[182:185], v[230:233], v[32:35]
	s_setprio 0
	s_setprio 1
	v_mfma_f32_16x16x32_bf16 v[124:127], v[186:189], v[202:205], v[124:127]
	v_mfma_f32_16x16x32_bf16 v[120:123], v[194:197], v[202:205], v[120:123]
	v_mfma_f32_16x16x32_bf16 v[116:119], v[186:189], v[210:213], v[116:119]
	v_mfma_f32_16x16x32_bf16 v[112:115], v[194:197], v[210:213], v[112:115]
	v_mfma_f32_16x16x32_bf16 v[108:111], v[186:189], v[218:221], v[108:111]
	v_mfma_f32_16x16x32_bf16 v[104:107], v[194:197], v[218:221], v[104:107]
	v_mfma_f32_16x16x32_bf16 v[100:103], v[186:189], v[226:229], v[100:103]
	v_mfma_f32_16x16x32_bf16 v[96:99], v[194:197], v[226:229], v[96:99]
	v_mfma_f32_16x16x32_bf16 v[124:127], v[190:193], v[206:209], v[124:127]
	v_mfma_f32_16x16x32_bf16 v[120:123], v[198:201], v[206:209], v[120:123]
	v_mfma_f32_16x16x32_bf16 v[116:119], v[190:193], v[214:217], v[116:119]
	v_mfma_f32_16x16x32_bf16 v[112:115], v[198:201], v[214:217], v[112:115]
	v_mfma_f32_16x16x32_bf16 v[108:111], v[190:193], v[222:225], v[108:111]
	v_mfma_f32_16x16x32_bf16 v[104:107], v[198:201], v[222:225], v[104:107]
	v_mfma_f32_16x16x32_bf16 v[100:103], v[190:193], v[230:233], v[100:103]
	v_mfma_f32_16x16x32_bf16 v[96:99], v[198:201], v[230:233], v[96:99]
	s_setprio 0
	s_barrier
	s_add_i32 s71, s66, s0
	v_lshl_add_u64 v[234:235], s[52:53], 0, v[136:137]
	s_mov_b32 m0, s71
	ds_read_b128 v[202:205], v165 offset:16384
	ds_read_b128 v[206:209], v165 offset:17408
	ds_read_b128 v[210:213], v165 offset:18432
	ds_read_b128 v[214:217], v165 offset:19456
	ds_read_b128 v[218:221], v165 offset:20480
	ds_read_b128 v[222:225], v165 offset:21504
	ds_read_b128 v[226:229], v165 offset:22528
	ds_read_b128 v[230:233], v165 offset:23552
	global_load_lds_dwordx4 v[234:235], off
	s_add_i32 m0, s71, 0x2000
	s_add_u32 s72, s52, 0x80000
	v_lshl_add_u64 v[236:237], s[52:53], 0, v[138:139]
	s_addc_u32 s73, s53, 0
	s_add_i32 s71, s67, s0
	global_load_lds_dwordx4 v[236:237], off
	v_lshl_add_u64 v[238:239], s[72:73], 0, v[136:137]
	s_mov_b32 m0, s71
	v_mov_b32_e32 v155, v141
	global_load_lds_dwordx4 v[238:239], off
	v_lshl_add_u64 v[238:239], s[72:73], 0, v[138:139]
	s_add_i32 m0, s71, 0x2000
	s_nop 0
	global_load_lds_dwordx4 v[238:239], off
	s_mov_b32 m0, s1
	v_lshl_add_u64 v[238:239], s[54:55], 0, v[140:141]
	global_load_lds_dwordx4 v140, s[54:55]
	s_mov_b32 m0, s8
	s_nop 0
	global_load_lds_dwordx4 v154, s[54:55]
	s_waitcnt vmcnt(8)
	s_waitcnt lgkmcnt(0)
	v_lshl_add_u64 v[154:155], s[54:55], 0, v[154:155]
	s_barrier
	s_setprio 1
	v_mfma_f32_16x16x32_bf16 v[28:31], v[170:173], v[202:205], v[28:31]
	v_mfma_f32_16x16x32_bf16 v[24:27], v[178:181], v[202:205], v[24:27]
	v_mfma_f32_16x16x32_bf16 v[20:23], v[170:173], v[210:213], v[20:23]
	v_mfma_f32_16x16x32_bf16 v[16:19], v[178:181], v[210:213], v[16:19]
	v_mfma_f32_16x16x32_bf16 v[12:15], v[170:173], v[218:221], v[12:15]
	v_mfma_f32_16x16x32_bf16 v[8:11], v[178:181], v[218:221], v[8:11]
	v_mfma_f32_16x16x32_bf16 v[4:7], v[170:173], v[226:229], v[4:7]
	v_mfma_f32_16x16x32_bf16 v[0:3], v[178:181], v[226:229], v[0:3]
	v_mfma_f32_16x16x32_bf16 v[28:31], v[174:177], v[206:209], v[28:31]
	v_mfma_f32_16x16x32_bf16 v[24:27], v[182:185], v[206:209], v[24:27]
	v_mfma_f32_16x16x32_bf16 v[20:23], v[174:177], v[214:217], v[20:23]
	v_mfma_f32_16x16x32_bf16 v[16:19], v[182:185], v[214:217], v[16:19]
	v_mfma_f32_16x16x32_bf16 v[12:15], v[174:177], v[222:225], v[12:15]
	v_mfma_f32_16x16x32_bf16 v[8:11], v[182:185], v[222:225], v[8:11]
	v_mfma_f32_16x16x32_bf16 v[4:7], v[174:177], v[230:233], v[4:7]
	v_mfma_f32_16x16x32_bf16 v[0:3], v[182:185], v[230:233], v[0:3]
	s_setprio 0
	s_setprio 1
	v_mfma_f32_16x16x32_bf16 v[92:95], v[186:189], v[202:205], v[92:95]
	v_mfma_f32_16x16x32_bf16 v[88:91], v[194:197], v[202:205], v[88:91]
	v_mfma_f32_16x16x32_bf16 v[84:87], v[186:189], v[210:213], v[84:87]
	v_mfma_f32_16x16x32_bf16 v[80:83], v[194:197], v[210:213], v[80:83]
	v_mfma_f32_16x16x32_bf16 v[72:75], v[186:189], v[218:221], v[72:75]
	v_mfma_f32_16x16x32_bf16 v[76:79], v[194:197], v[218:221], v[76:79]
	v_mfma_f32_16x16x32_bf16 v[64:67], v[186:189], v[226:229], v[64:67]
	v_mfma_f32_16x16x32_bf16 v[68:71], v[194:197], v[226:229], v[68:71]
	v_mfma_f32_16x16x32_bf16 v[92:95], v[190:193], v[206:209], v[92:95]
	v_mfma_f32_16x16x32_bf16 v[88:91], v[198:201], v[206:209], v[88:91]
	v_mfma_f32_16x16x32_bf16 v[84:87], v[190:193], v[214:217], v[84:87]
	v_mfma_f32_16x16x32_bf16 v[80:83], v[198:201], v[214:217], v[80:83]
	v_mfma_f32_16x16x32_bf16 v[72:75], v[190:193], v[222:225], v[72:75]
	v_mfma_f32_16x16x32_bf16 v[76:79], v[198:201], v[222:225], v[76:79]
	v_mfma_f32_16x16x32_bf16 v[64:67], v[190:193], v[230:233], v[64:67]
	v_mfma_f32_16x16x32_bf16 v[68:71], v[198:201], v[230:233], v[68:71]
	s_setprio 0
	s_barrier
	s_add_i32 s71, 0, 0x18000
	v_add_u32_e32 v133, s71, v161
	s_add_i32 s72, 0, 0x1c000
	ds_read_b128 v[170:173], v133
	ds_read_b128 v[174:177], v133 offset:1024
	ds_read_b128 v[178:181], v133 offset:2048
	ds_read_b128 v[182:185], v133 offset:3072
	v_add_u32_e32 v133, s72, v161
	ds_read_b128 v[186:189], v133
	ds_read_b128 v[190:193], v133 offset:1024
	ds_read_b128 v[194:197], v133 offset:2048
	ds_read_b128 v[198:201], v133 offset:3072
	s_mov_b32 m0, s9
	ds_read_b128 v[202:205], v165 offset:32768
	ds_read_b128 v[206:209], v165 offset:33792
	ds_read_b128 v[210:213], v165 offset:34816
	ds_read_b128 v[214:217], v165 offset:35840
	ds_read_b128 v[218:221], v165 offset:36864
	ds_read_b128 v[222:225], v165 offset:37888
	ds_read_b128 v[226:229], v165 offset:38912
	ds_read_b128 v[230:233], v165 offset:39936
	global_load_lds_dwordx4 v129, s[54:55]
	s_mov_b32 m0, s31
	s_nop 0
	global_load_lds_dwordx4 v131, s[54:55]
	s_waitcnt vmcnt(8)
	s_waitcnt lgkmcnt(0)
	s_barrier
	s_setprio 1
	v_mfma_f32_16x16x32_bf16 v[60:63], v[170:173], v[202:205], v[60:63]
	v_mfma_f32_16x16x32_bf16 v[56:59], v[178:181], v[202:205], v[56:59]
	v_mfma_f32_16x16x32_bf16 v[52:55], v[170:173], v[210:213], v[52:55]
	v_mfma_f32_16x16x32_bf16 v[48:51], v[178:181], v[210:213], v[48:51]
	v_mfma_f32_16x16x32_bf16 v[44:47], v[170:173], v[218:221], v[44:47]
	v_mfma_f32_16x16x32_bf16 v[40:43], v[178:181], v[218:221], v[40:43]
	v_mfma_f32_16x16x32_bf16 v[36:39], v[170:173], v[226:229], v[36:39]
	v_mfma_f32_16x16x32_bf16 v[32:35], v[178:181], v[226:229], v[32:35]
	v_mfma_f32_16x16x32_bf16 v[60:63], v[174:177], v[206:209], v[60:63]
	v_mfma_f32_16x16x32_bf16 v[56:59], v[182:185], v[206:209], v[56:59]
	v_mfma_f32_16x16x32_bf16 v[52:55], v[174:177], v[214:217], v[52:55]
	v_mfma_f32_16x16x32_bf16 v[48:51], v[182:185], v[214:217], v[48:51]
	v_mfma_f32_16x16x32_bf16 v[44:47], v[174:177], v[222:225], v[44:47]
	v_mfma_f32_16x16x32_bf16 v[40:43], v[182:185], v[222:225], v[40:43]
	v_mfma_f32_16x16x32_bf16 v[36:39], v[174:177], v[230:233], v[36:39]
	v_mfma_f32_16x16x32_bf16 v[32:35], v[182:185], v[230:233], v[32:35]
	s_setprio 0
	s_setprio 1
	v_mfma_f32_16x16x32_bf16 v[124:127], v[186:189], v[202:205], v[124:127]
	v_mfma_f32_16x16x32_bf16 v[120:123], v[194:197], v[202:205], v[120:123]
	v_mfma_f32_16x16x32_bf16 v[116:119], v[186:189], v[210:213], v[116:119]
	v_mfma_f32_16x16x32_bf16 v[112:115], v[194:197], v[210:213], v[112:115]
	v_mfma_f32_16x16x32_bf16 v[108:111], v[186:189], v[218:221], v[108:111]
	v_mfma_f32_16x16x32_bf16 v[104:107], v[194:197], v[218:221], v[104:107]
	v_mfma_f32_16x16x32_bf16 v[100:103], v[186:189], v[226:229], v[100:103]
	v_mfma_f32_16x16x32_bf16 v[96:99], v[194:197], v[226:229], v[96:99]
	v_mfma_f32_16x16x32_bf16 v[124:127], v[190:193], v[206:209], v[124:127]
	v_mfma_f32_16x16x32_bf16 v[120:123], v[198:201], v[206:209], v[120:123]
	v_mfma_f32_16x16x32_bf16 v[116:119], v[190:193], v[214:217], v[116:119]
	v_mfma_f32_16x16x32_bf16 v[112:115], v[198:201], v[214:217], v[112:115]
	v_mfma_f32_16x16x32_bf16 v[108:111], v[190:193], v[222:225], v[108:111]
	v_mfma_f32_16x16x32_bf16 v[104:107], v[198:201], v[222:225], v[104:107]
	v_mfma_f32_16x16x32_bf16 v[100:103], v[190:193], v[230:233], v[100:103]
	v_mfma_f32_16x16x32_bf16 v[96:99], v[198:201], v[230:233], v[96:99]
	s_setprio 0
	s_barrier
	s_add_i32 s54, s71, s0
	v_lshl_add_u64 v[234:235], v[234:235], 0, s[24:25]
	s_mov_b32 m0, s54
	ds_read_b128 v[202:205], v165 offset:49152
	ds_read_b128 v[206:209], v165 offset:50176
	ds_read_b128 v[210:213], v165 offset:51200
	ds_read_b128 v[214:217], v165 offset:52224
	ds_read_b128 v[218:221], v165 offset:53248
	ds_read_b128 v[222:225], v165 offset:54272
	ds_read_b128 v[226:229], v165 offset:55296
	ds_read_b128 v[230:233], v165 offset:56320
	global_load_lds_dwordx4 v[234:235], off
	s_add_i32 m0, s54, 0x2000
	s_add_u32 s52, s52, 0x80080
	v_lshl_add_u64 v[234:235], v[236:237], 0, s[24:25]
	s_addc_u32 s53, s53, 0
	s_add_i32 s54, s72, s0
	global_load_lds_dwordx4 v[234:235], off
	v_lshl_add_u64 v[234:235], s[52:53], 0, v[136:137]
	s_mov_b32 m0, s54
	v_lshl_add_u64 v[154:155], v[154:155], 0, s[24:25]
	global_load_lds_dwordx4 v[234:235], off
	v_lshl_add_u64 v[234:235], s[52:53], 0, v[138:139]
	s_add_i32 m0, s54, 0x2000
	s_nop 0
	global_load_lds_dwordx4 v[234:235], off
	v_lshl_add_u64 v[234:235], v[238:239], 0, s[24:25]
	s_mov_b32 m0, s60
	s_nop 0
	global_load_lds_dwordx4 v[234:235], off
	s_mov_b32 m0, s61
	s_nop 0
	global_load_lds_dwordx4 v[154:155], off
	s_waitcnt vmcnt(8)
	s_waitcnt lgkmcnt(0)
	s_barrier
	s_setprio 1
	v_mfma_f32_16x16x32_bf16 v[28:31], v[170:173], v[202:205], v[28:31]
	v_mfma_f32_16x16x32_bf16 v[24:27], v[178:181], v[202:205], v[24:27]
	v_mfma_f32_16x16x32_bf16 v[20:23], v[170:173], v[210:213], v[20:23]
	v_mfma_f32_16x16x32_bf16 v[16:19], v[178:181], v[210:213], v[16:19]
	v_mfma_f32_16x16x32_bf16 v[12:15], v[170:173], v[218:221], v[12:15]
	v_mfma_f32_16x16x32_bf16 v[8:11], v[178:181], v[218:221], v[8:11]
	v_mfma_f32_16x16x32_bf16 v[4:7], v[170:173], v[226:229], v[4:7]
	v_mfma_f32_16x16x32_bf16 v[0:3], v[178:181], v[226:229], v[0:3]
	v_mfma_f32_16x16x32_bf16 v[28:31], v[174:177], v[206:209], v[28:31]
	v_mfma_f32_16x16x32_bf16 v[24:27], v[182:185], v[206:209], v[24:27]
	v_mfma_f32_16x16x32_bf16 v[20:23], v[174:177], v[214:217], v[20:23]
	v_mfma_f32_16x16x32_bf16 v[16:19], v[182:185], v[214:217], v[16:19]
	v_mfma_f32_16x16x32_bf16 v[12:15], v[174:177], v[222:225], v[12:15]
	v_mfma_f32_16x16x32_bf16 v[8:11], v[182:185], v[222:225], v[8:11]
	v_mfma_f32_16x16x32_bf16 v[4:7], v[174:177], v[230:233], v[4:7]
	v_mfma_f32_16x16x32_bf16 v[0:3], v[182:185], v[230:233], v[0:3]
	s_setprio 0
	s_setprio 1
	v_mfma_f32_16x16x32_bf16 v[92:95], v[186:189], v[202:205], v[92:95]
	v_mfma_f32_16x16x32_bf16 v[88:91], v[194:197], v[202:205], v[88:91]
	v_mfma_f32_16x16x32_bf16 v[84:87], v[186:189], v[210:213], v[84:87]
	v_mfma_f32_16x16x32_bf16 v[80:83], v[194:197], v[210:213], v[80:83]
	v_mfma_f32_16x16x32_bf16 v[72:75], v[186:189], v[218:221], v[72:75]
	v_mfma_f32_16x16x32_bf16 v[76:79], v[194:197], v[218:221], v[76:79]
	v_mfma_f32_16x16x32_bf16 v[64:67], v[186:189], v[226:229], v[64:67]
	v_mfma_f32_16x16x32_bf16 v[68:71], v[194:197], v[226:229], v[68:71]
	v_mfma_f32_16x16x32_bf16 v[92:95], v[190:193], v[206:209], v[92:95]
	v_mfma_f32_16x16x32_bf16 v[88:91], v[198:201], v[206:209], v[88:91]
	v_mfma_f32_16x16x32_bf16 v[84:87], v[190:193], v[214:217], v[84:87]
	v_mfma_f32_16x16x32_bf16 v[80:83], v[198:201], v[214:217], v[80:83]
	v_mfma_f32_16x16x32_bf16 v[72:75], v[190:193], v[222:225], v[72:75]
	v_mfma_f32_16x16x32_bf16 v[76:79], v[198:201], v[222:225], v[76:79]
	v_mfma_f32_16x16x32_bf16 v[64:67], v[190:193], v[230:233], v[64:67]
	v_mfma_f32_16x16x32_bf16 v[68:71], v[198:201], v[230:233], v[68:71]
	s_setprio 0
	s_add_i32 s70, s70, 2
	s_add_u32 s4, s4, 0x100
	s_addc_u32 s5, s5, 0
	s_cmp_gt_u32 s70, 29
	s_barrier
	s_cbranch_scc0 .LBB0_180
	s_and_b64 vcc, exec, s[26:27]
	s_cbranch_vccnz .LBB0_184
	v_lshl_add_u32 v150, s62, 8, v160
	s_cmp_lg_u32 s6, 46
	s_mov_b64 s[4:5], -1
	s_cbranch_scc1 .LBB0_185

.LBB0_888:
	s_add_i32 s63, s38, 2
	s_add_u32 s39, s30, s36
	s_addc_u32 s40, s31, s37
	v_add_u32_e32 v131, s44, v152
	s_add_u32 s64, s39, 0x100
	ds_read_b128 v[160:163], v131
	ds_read_b128 v[164:167], v131 offset:1024
	ds_read_b128 v[168:171], v131 offset:2048
	ds_read_b128 v[172:175], v131 offset:3072
	v_add_u32_e32 v131, s45, v152
	s_addc_u32 s40, s40, 0
	ds_read_b128 v[176:179], v131
	ds_read_b128 v[180:183], v131 offset:1024
	ds_read_b128 v[184:187], v131 offset:2048
	ds_read_b128 v[188:191], v131 offset:3072
	s_add_u32 s65, s61, s36
	s_addc_u32 s66, s62, s37
	s_cmp_eq_u32 s60, s38
	s_cselect_b64 vcc, -1, 0
	s_and_b64 s[38:39], vcc, exec
	s_cselect_b32 s38, s55, s65
	v_cndmask_b32_e32 v136, v128, v156, vcc
	s_cselect_b32 s41, s57, s40
	s_cselect_b32 s40, s59, s64
	v_cndmask_b32_e32 v129, v138, v158, vcc
	v_cndmask_b32_e32 v224, v130, v157, vcc
	v_cndmask_b32_e32 v131, v140, v159, vcc
	s_cselect_b32 s39, s25, s66
	v_lshl_add_u64 v[226:227], v[146:147], 0, s[36:37]
	s_add_i32 m0, s1, 0xc000
	ds_read_b128 v[192:195], v155
	ds_read_b128 v[196:199], v155 offset:1024
	ds_read_b128 v[200:203], v155 offset:2048
	ds_read_b128 v[204:207], v155 offset:3072
	ds_read_b128 v[208:211], v155 offset:4096
	ds_read_b128 v[212:215], v155 offset:5120
	ds_read_b128 v[216:219], v155 offset:6144
	ds_read_b128 v[220:223], v155 offset:7168
	global_load_lds_dwordx4 v[226:227], off
	v_lshl_add_u64 v[226:227], v[142:143], 0, s[36:37]
	s_add_i32 m0, s1, 0xe000
	s_nop 0
	global_load_lds_dwordx4 v[226:227], off
	s_waitcnt vmcnt(8)
	s_waitcnt lgkmcnt(0)
	s_barrier
	s_setprio 1
	v_mfma_f32_16x16x32_bf16 v[108:111], v[160:163], v[192:195], v[108:111]
	v_mfma_f32_16x16x32_bf16 v[104:107], v[168:171], v[192:195], v[104:107]
	v_mfma_f32_16x16x32_bf16 v[100:103], v[160:163], v[200:203], v[100:103]
	v_mfma_f32_16x16x32_bf16 v[96:99], v[168:171], v[200:203], v[96:99]
	v_mfma_f32_16x16x32_bf16 v[92:95], v[160:163], v[208:211], v[92:95]
	v_mfma_f32_16x16x32_bf16 v[88:91], v[168:171], v[208:211], v[88:91]
	v_mfma_f32_16x16x32_bf16 v[84:87], v[160:163], v[216:219], v[84:87]
	v_mfma_f32_16x16x32_bf16 v[80:83], v[168:171], v[216:219], v[80:83]
	v_mfma_f32_16x16x32_bf16 v[108:111], v[164:167], v[196:199], v[108:111]
	v_mfma_f32_16x16x32_bf16 v[104:107], v[172:175], v[196:199], v[104:107]
	v_mfma_f32_16x16x32_bf16 v[100:103], v[164:167], v[204:207], v[100:103]
	v_mfma_f32_16x16x32_bf16 v[96:99], v[172:175], v[204:207], v[96:99]
	v_mfma_f32_16x16x32_bf16 v[92:95], v[164:167], v[212:215], v[92:95]
	v_mfma_f32_16x16x32_bf16 v[88:91], v[172:175], v[212:215], v[88:91]
	v_mfma_f32_16x16x32_bf16 v[84:87], v[164:167], v[220:223], v[84:87]
	v_mfma_f32_16x16x32_bf16 v[80:83], v[172:175], v[220:223], v[80:83]
	s_setprio 0
	s_setprio 1
	v_mfma_f32_16x16x32_bf16 v[76:79], v[176:179], v[192:195], v[76:79]
	v_mfma_f32_16x16x32_bf16 v[72:75], v[184:187], v[192:195], v[72:75]
	v_mfma_f32_16x16x32_bf16 v[68:71], v[176:179], v[200:203], v[68:71]
	v_mfma_f32_16x16x32_bf16 v[64:67], v[184:187], v[200:203], v[64:67]
	v_mfma_f32_16x16x32_bf16 v[60:63], v[176:179], v[208:211], v[60:63]
	v_mfma_f32_16x16x32_bf16 v[56:59], v[184:187], v[208:211], v[56:59]
	v_mfma_f32_16x16x32_bf16 v[52:55], v[176:179], v[216:219], v[52:55]
	v_mfma_f32_16x16x32_bf16 v[48:51], v[184:187], v[216:219], v[48:51]
	v_mfma_f32_16x16x32_bf16 v[76:79], v[180:183], v[196:199], v[76:79]
	v_mfma_f32_16x16x32_bf16 v[72:75], v[188:191], v[196:199], v[72:75]
	v_mfma_f32_16x16x32_bf16 v[68:71], v[180:183], v[204:207], v[68:71]
	v_mfma_f32_16x16x32_bf16 v[64:67], v[188:191], v[204:207], v[64:67]
	v_mfma_f32_16x16x32_bf16 v[60:63], v[180:183], v[212:215], v[60:63]
	v_mfma_f32_16x16x32_bf16 v[56:59], v[188:191], v[212:215], v[56:59]
	v_mfma_f32_16x16x32_bf16 v[52:55], v[180:183], v[220:223], v[52:55]
	v_mfma_f32_16x16x32_bf16 v[48:51], v[188:191], v[220:223], v[48:51]
	s_setprio 0
	s_barrier
	s_add_i32 s64, s44, s0
	v_lshl_add_u64 v[226:227], s[38:39], 0, v[132:133]
	s_mov_b32 m0, s64
	ds_read_b128 v[192:195], v155 offset:16384
	ds_read_b128 v[196:199], v155 offset:17408
	ds_read_b128 v[200:203], v155 offset:18432
	ds_read_b128 v[204:207], v155 offset:19456
	ds_read_b128 v[208:211], v155 offset:20480
	ds_read_b128 v[212:215], v155 offset:21504
	ds_read_b128 v[216:219], v155 offset:22528
	ds_read_b128 v[220:223], v155 offset:23552
	global_load_lds_dwordx4 v[226:227], off
	s_add_i32 m0, s64, 0x2000
	s_add_u32 s64, s38, 0x80000
	v_lshl_add_u64 v[228:229], s[38:39], 0, v[134:135]
	s_addc_u32 s65, s39, 0
	s_add_i32 s66, s45, s0
	global_load_lds_dwordx4 v[228:229], off
	v_lshl_add_u64 v[230:231], s[64:65], 0, v[132:133]
	s_mov_b32 m0, s66
	v_mov_b32_e32 v225, v137
	global_load_lds_dwordx4 v[230:231], off
	v_lshl_add_u64 v[230:231], s[64:65], 0, v[134:135]
	s_add_i32 m0, s66, 0x2000
	s_nop 0
	global_load_lds_dwordx4 v[230:231], off
	s_mov_b32 m0, s1
	v_lshl_add_u64 v[230:231], s[40:41], 0, v[136:137]
	global_load_lds_dwordx4 v136, s[40:41]
	s_mov_b32 m0, s4
	s_nop 0
	global_load_lds_dwordx4 v224, s[40:41]
	s_waitcnt vmcnt(8)
	s_waitcnt lgkmcnt(0)
	v_lshl_add_u64 v[224:225], s[40:41], 0, v[224:225]
	s_barrier
	s_setprio 1
	v_mfma_f32_16x16x32_bf16 v[44:47], v[160:163], v[192:195], v[44:47]
	v_mfma_f32_16x16x32_bf16 v[40:43], v[168:171], v[192:195], v[40:43]
	v_mfma_f32_16x16x32_bf16 v[36:39], v[160:163], v[200:203], v[36:39]
	v_mfma_f32_16x16x32_bf16 v[32:35], v[168:171], v[200:203], v[32:35]
	v_mfma_f32_16x16x32_bf16 v[28:31], v[160:163], v[208:211], v[28:31]
	v_mfma_f32_16x16x32_bf16 v[24:27], v[168:171], v[208:211], v[24:27]
	v_mfma_f32_16x16x32_bf16 v[20:23], v[160:163], v[216:219], v[20:23]
	v_mfma_f32_16x16x32_bf16 v[16:19], v[168:171], v[216:219], v[16:19]
	v_mfma_f32_16x16x32_bf16 v[44:47], v[164:167], v[196:199], v[44:47]
	v_mfma_f32_16x16x32_bf16 v[40:43], v[172:175], v[196:199], v[40:43]
	v_mfma_f32_16x16x32_bf16 v[36:39], v[164:167], v[204:207], v[36:39]
	v_mfma_f32_16x16x32_bf16 v[32:35], v[172:175], v[204:207], v[32:35]
	v_mfma_f32_16x16x32_bf16 v[28:31], v[164:167], v[212:215], v[28:31]
	v_mfma_f32_16x16x32_bf16 v[24:27], v[172:175], v[212:215], v[24:27]
	v_mfma_f32_16x16x32_bf16 v[20:23], v[164:167], v[220:223], v[20:23]
	v_mfma_f32_16x16x32_bf16 v[16:19], v[172:175], v[220:223], v[16:19]
	s_setprio 0
	s_setprio 1
	v_mfma_f32_16x16x32_bf16 v[12:15], v[176:179], v[192:195], v[12:15]
	v_mfma_f32_16x16x32_bf16 v[8:11], v[184:187], v[192:195], v[8:11]
	v_mfma_f32_16x16x32_bf16 v[4:7], v[176:179], v[200:203], v[4:7]
	v_mfma_f32_16x16x32_bf16 v[0:3], v[184:187], v[200:203], v[0:3]
	v_mfma_f32_16x16x32_bf16 v[112:115], v[176:179], v[208:211], v[112:115]
	v_mfma_f32_16x16x32_bf16 v[116:119], v[184:187], v[208:211], v[116:119]
	v_mfma_f32_16x16x32_bf16 v[120:123], v[176:179], v[216:219], v[120:123]
	v_mfma_f32_16x16x32_bf16 v[124:127], v[184:187], v[216:219], v[124:127]
	v_mfma_f32_16x16x32_bf16 v[12:15], v[180:183], v[196:199], v[12:15]
	v_mfma_f32_16x16x32_bf16 v[8:11], v[188:191], v[196:199], v[8:11]
	v_mfma_f32_16x16x32_bf16 v[4:7], v[180:183], v[204:207], v[4:7]
	v_mfma_f32_16x16x32_bf16 v[0:3], v[188:191], v[204:207], v[0:3]
	v_mfma_f32_16x16x32_bf16 v[112:115], v[180:183], v[212:215], v[112:115]
	v_mfma_f32_16x16x32_bf16 v[116:119], v[188:191], v[212:215], v[116:119]
	v_mfma_f32_16x16x32_bf16 v[120:123], v[180:183], v[220:223], v[120:123]
	v_mfma_f32_16x16x32_bf16 v[124:127], v[188:191], v[220:223], v[124:127]
	s_setprio 0
	s_barrier
	s_add_i32 s64, 0, 0x18000
	v_add_u32_e32 v136, s64, v152
	s_add_i32 s65, 0, 0x1c000
	ds_read_b128 v[160:163], v136
	ds_read_b128 v[164:167], v136 offset:1024
	ds_read_b128 v[168:171], v136 offset:2048
	ds_read_b128 v[172:175], v136 offset:3072
	v_add_u32_e32 v136, s65, v152
	ds_read_b128 v[176:179], v136
	ds_read_b128 v[180:183], v136 offset:1024
	ds_read_b128 v[184:187], v136 offset:2048
	ds_read_b128 v[188:191], v136 offset:3072
	s_mov_b32 m0, s5
	ds_read_b128 v[192:195], v155 offset:32768
	ds_read_b128 v[196:199], v155 offset:33792
	ds_read_b128 v[200:203], v155 offset:34816
	ds_read_b128 v[204:207], v155 offset:35840
	ds_read_b128 v[208:211], v155 offset:36864
	ds_read_b128 v[212:215], v155 offset:37888
	ds_read_b128 v[216:219], v155 offset:38912
	ds_read_b128 v[220:223], v155 offset:39936
	global_load_lds_dwordx4 v129, s[40:41]
	s_mov_b32 m0, s6
	s_nop 0
	global_load_lds_dwordx4 v131, s[40:41]
	s_waitcnt vmcnt(8)
	s_waitcnt lgkmcnt(0)
	s_barrier
	s_setprio 1
	v_mfma_f32_16x16x32_bf16 v[108:111], v[160:163], v[192:195], v[108:111]
	v_mfma_f32_16x16x32_bf16 v[104:107], v[168:171], v[192:195], v[104:107]
	v_mfma_f32_16x16x32_bf16 v[100:103], v[160:163], v[200:203], v[100:103]
	v_mfma_f32_16x16x32_bf16 v[96:99], v[168:171], v[200:203], v[96:99]
	v_mfma_f32_16x16x32_bf16 v[92:95], v[160:163], v[208:211], v[92:95]
	v_mfma_f32_16x16x32_bf16 v[88:91], v[168:171], v[208:211], v[88:91]
	v_mfma_f32_16x16x32_bf16 v[84:87], v[160:163], v[216:219], v[84:87]
	v_mfma_f32_16x16x32_bf16 v[80:83], v[168:171], v[216:219], v[80:83]
	v_mfma_f32_16x16x32_bf16 v[108:111], v[164:167], v[196:199], v[108:111]
	v_mfma_f32_16x16x32_bf16 v[104:107], v[172:175], v[196:199], v[104:107]
	v_mfma_f32_16x16x32_bf16 v[100:103], v[164:167], v[204:207], v[100:103]
	v_mfma_f32_16x16x32_bf16 v[96:99], v[172:175], v[204:207], v[96:99]
	v_mfma_f32_16x16x32_bf16 v[92:95], v[164:167], v[212:215], v[92:95]
	v_mfma_f32_16x16x32_bf16 v[88:91], v[172:175], v[212:215], v[88:91]
	v_mfma_f32_16x16x32_bf16 v[84:87], v[164:167], v[220:223], v[84:87]
	v_mfma_f32_16x16x32_bf16 v[80:83], v[172:175], v[220:223], v[80:83]
	s_setprio 0
	s_setprio 1
	v_mfma_f32_16x16x32_bf16 v[76:79], v[176:179], v[192:195], v[76:79]
	v_mfma_f32_16x16x32_bf16 v[72:75], v[184:187], v[192:195], v[72:75]
	v_mfma_f32_16x16x32_bf16 v[68:71], v[176:179], v[200:203], v[68:71]
	v_mfma_f32_16x16x32_bf16 v[64:67], v[184:187], v[200:203], v[64:67]
	v_mfma_f32_16x16x32_bf16 v[60:63], v[176:179], v[208:211], v[60:63]
	v_mfma_f32_16x16x32_bf16 v[56:59], v[184:187], v[208:211], v[56:59]
	v_mfma_f32_16x16x32_bf16 v[52:55], v[176:179], v[216:219], v[52:55]
	v_mfma_f32_16x16x32_bf16 v[48:51], v[184:187], v[216:219], v[48:51]
	v_mfma_f32_16x16x32_bf16 v[76:79], v[180:183], v[196:199], v[76:79]
	v_mfma_f32_16x16x32_bf16 v[72:75], v[188:191], v[196:199], v[72:75]
	v_mfma_f32_16x16x32_bf16 v[68:71], v[180:183], v[204:207], v[68:71]
	v_mfma_f32_16x16x32_bf16 v[64:67], v[188:191], v[204:207], v[64:67]
	v_mfma_f32_16x16x32_bf16 v[60:63], v[180:183], v[212:215], v[60:63]
	v_mfma_f32_16x16x32_bf16 v[56:59], v[188:191], v[212:215], v[56:59]
	v_mfma_f32_16x16x32_bf16 v[52:55], v[180:183], v[220:223], v[52:55]
	v_mfma_f32_16x16x32_bf16 v[48:51], v[188:191], v[220:223], v[48:51]
	s_setprio 0
	s_barrier
	s_add_i32 s40, s64, s0
	v_lshl_add_u64 v[226:227], v[226:227], 0, s[18:19]
	s_mov_b32 m0, s40
	ds_read_b128 v[192:195], v155 offset:49152
	ds_read_b128 v[196:199], v155 offset:50176
	ds_read_b128 v[200:203], v155 offset:51200
	ds_read_b128 v[204:207], v155 offset:52224
	ds_read_b128 v[208:211], v155 offset:53248
	ds_read_b128 v[212:215], v155 offset:54272
	ds_read_b128 v[216:219], v155 offset:55296
	ds_read_b128 v[220:223], v155 offset:56320
	global_load_lds_dwordx4 v[226:227], off
	s_add_i32 m0, s40, 0x2000
	s_add_u32 s38, s38, 0x80080
	v_lshl_add_u64 v[226:227], v[228:229], 0, s[18:19]
	s_addc_u32 s39, s39, 0
	s_add_i32 s40, s65, s0
	global_load_lds_dwordx4 v[226:227], off
	v_lshl_add_u64 v[226:227], s[38:39], 0, v[132:133]
	s_mov_b32 m0, s40
	v_lshl_add_u64 v[224:225], v[224:225], 0, s[18:19]
	global_load_lds_dwordx4 v[226:227], off
	v_lshl_add_u64 v[226:227], s[38:39], 0, v[134:135]
	s_add_i32 m0, s40, 0x2000
	s_nop 0
	global_load_lds_dwordx4 v[226:227], off
	v_lshl_add_u64 v[226:227], v[230:231], 0, s[18:19]
	s_mov_b32 m0, s9
	s_nop 0
	global_load_lds_dwordx4 v[226:227], off
	s_mov_b32 m0, s42
	s_nop 0
	global_load_lds_dwordx4 v[224:225], off
	s_waitcnt vmcnt(8)
	s_waitcnt lgkmcnt(0)
	s_barrier
	s_setprio 1
	v_mfma_f32_16x16x32_bf16 v[44:47], v[160:163], v[192:195], v[44:47]
	v_mfma_f32_16x16x32_bf16 v[40:43], v[168:171], v[192:195], v[40:43]
	v_mfma_f32_16x16x32_bf16 v[36:39], v[160:163], v[200:203], v[36:39]
	v_mfma_f32_16x16x32_bf16 v[32:35], v[168:171], v[200:203], v[32:35]
	v_mfma_f32_16x16x32_bf16 v[28:31], v[160:163], v[208:211], v[28:31]
	v_mfma_f32_16x16x32_bf16 v[24:27], v[168:171], v[208:211], v[24:27]
	v_mfma_f32_16x16x32_bf16 v[20:23], v[160:163], v[216:219], v[20:23]
	v_mfma_f32_16x16x32_bf16 v[16:19], v[168:171], v[216:219], v[16:19]
	v_mfma_f32_16x16x32_bf16 v[44:47], v[164:167], v[196:199], v[44:47]
	v_mfma_f32_16x16x32_bf16 v[40:43], v[172:175], v[196:199], v[40:43]
	v_mfma_f32_16x16x32_bf16 v[36:39], v[164:167], v[204:207], v[36:39]
	v_mfma_f32_16x16x32_bf16 v[32:35], v[172:175], v[204:207], v[32:35]
	v_mfma_f32_16x16x32_bf16 v[28:31], v[164:167], v[212:215], v[28:31]
	v_mfma_f32_16x16x32_bf16 v[24:27], v[172:175], v[212:215], v[24:27]
	v_mfma_f32_16x16x32_bf16 v[20:23], v[164:167], v[220:223], v[20:23]
	v_mfma_f32_16x16x32_bf16 v[16:19], v[172:175], v[220:223], v[16:19]
	s_setprio 0
	s_setprio 1
	v_mfma_f32_16x16x32_bf16 v[12:15], v[176:179], v[192:195], v[12:15]
	v_mfma_f32_16x16x32_bf16 v[8:11], v[184:187], v[192:195], v[8:11]
	v_mfma_f32_16x16x32_bf16 v[4:7], v[176:179], v[200:203], v[4:7]
	v_mfma_f32_16x16x32_bf16 v[0:3], v[184:187], v[200:203], v[0:3]
	v_mfma_f32_16x16x32_bf16 v[112:115], v[176:179], v[208:211], v[112:115]
	v_mfma_f32_16x16x32_bf16 v[116:119], v[184:187], v[208:211], v[116:119]
	v_mfma_f32_16x16x32_bf16 v[120:123], v[176:179], v[216:219], v[120:123]
	v_mfma_f32_16x16x32_bf16 v[124:127], v[184:187], v[216:219], v[124:127]
	v_mfma_f32_16x16x32_bf16 v[12:15], v[180:183], v[196:199], v[12:15]
	v_mfma_f32_16x16x32_bf16 v[8:11], v[188:191], v[196:199], v[8:11]
	v_mfma_f32_16x16x32_bf16 v[4:7], v[180:183], v[204:207], v[4:7]
	v_mfma_f32_16x16x32_bf16 v[0:3], v[188:191], v[204:207], v[0:3]
	v_mfma_f32_16x16x32_bf16 v[112:115], v[180:183], v[212:215], v[112:115]
	v_mfma_f32_16x16x32_bf16 v[116:119], v[188:191], v[212:215], v[116:119]
	v_mfma_f32_16x16x32_bf16 v[120:123], v[180:183], v[220:223], v[120:123]
	v_mfma_f32_16x16x32_bf16 v[124:127], v[188:191], v[220:223], v[124:127]
	s_setprio 0
	s_add_u32 s36, s36, 0x100
	s_addc_u32 s37, s37, 0
	s_cmp_ge_i32 s63, s53
	s_mov_b32 s38, s63
	s_barrier
	s_cbranch_scc0 .LBB0_888
	s_and_b64 vcc, exec, s[20:21]
	s_cbranch_vccz .LBB0_891
	s_barrier

.LBB0_964:
	ds_read_b128 v[140:143], v162
	ds_read_b128 v[170:173], v162 offset:1024
	ds_read_b128 v[174:177], v162 offset:2048
	ds_read_b128 v[178:181], v162 offset:3072
	ds_read_b128 v[182:185], v163
	ds_read_b128 v[186:189], v163 offset:1024
	ds_read_b128 v[190:193], v163 offset:2048
	ds_read_b128 v[194:197], v163 offset:3072
	s_add_u32 s46, s42, s12
	s_addc_u32 s47, s43, s13
	s_cmpk_eq_i32 s12, 0x1000
	s_cselect_b64 vcc, -1, 0
	s_and_b64 s[44:45], vcc, exec
	s_cselect_b32 s64, 0, s12
	s_cselect_b32 s63, 0, s13
	s_cselect_b32 s44, s61, s46
	s_cselect_b32 s45, s39, s47
	s_add_u32 s46, s14, s64
	v_cndmask_b32_e32 v150, v128, v165, vcc
	v_cndmask_b32_e32 v129, v132, v167, vcc
	v_cndmask_b32_e32 v230, v130, v166, vcc
	v_cndmask_b32_e32 v131, v134, v168, vcc
	s_addc_u32 s47, s15, s63
	v_lshl_add_u64 v[232:233], v[138:139], 0, s[12:13]
	v_lshl_add_u64 v[232:233], v[232:233], 0, s[28:29]
	s_add_i32 m0, s4, 0xc000
	ds_read_b128 v[198:201], v164
	ds_read_b128 v[202:205], v164 offset:1024
	ds_read_b128 v[206:209], v164 offset:2048
	ds_read_b128 v[210:213], v164 offset:3072
	ds_read_b128 v[214:217], v164 offset:4096
	ds_read_b128 v[218:221], v164 offset:5120
	ds_read_b128 v[222:225], v164 offset:6144
	ds_read_b128 v[226:229], v164 offset:7168
	global_load_lds_dwordx4 v[232:233], off
	v_lshl_add_u64 v[232:233], v[136:137], 0, s[12:13]
	v_lshl_add_u64 v[232:233], v[232:233], 0, s[28:29]
	s_add_i32 m0, s4, 0xe000
	s_nop 0
	global_load_lds_dwordx4 v[232:233], off
	s_waitcnt vmcnt(8)
	s_waitcnt lgkmcnt(0)
	s_barrier
	s_setprio 1
	v_mfma_f32_16x16x32_bf16 v[124:127], v[140:143], v[198:201], v[124:127]
	v_mfma_f32_16x16x32_bf16 v[120:123], v[174:177], v[198:201], v[120:123]
	v_mfma_f32_16x16x32_bf16 v[116:119], v[140:143], v[206:209], v[116:119]
	v_mfma_f32_16x16x32_bf16 v[112:115], v[174:177], v[206:209], v[112:115]
	v_mfma_f32_16x16x32_bf16 v[108:111], v[140:143], v[214:217], v[108:111]
	v_mfma_f32_16x16x32_bf16 v[100:103], v[174:177], v[214:217], v[100:103]
	v_mfma_f32_16x16x32_bf16 v[92:95], v[140:143], v[222:225], v[92:95]
	v_mfma_f32_16x16x32_bf16 v[84:87], v[174:177], v[222:225], v[84:87]
	v_mfma_f32_16x16x32_bf16 v[124:127], v[170:173], v[202:205], v[124:127]
	v_mfma_f32_16x16x32_bf16 v[120:123], v[178:181], v[202:205], v[120:123]
	v_mfma_f32_16x16x32_bf16 v[116:119], v[170:173], v[210:213], v[116:119]
	v_mfma_f32_16x16x32_bf16 v[112:115], v[178:181], v[210:213], v[112:115]
	v_mfma_f32_16x16x32_bf16 v[108:111], v[170:173], v[218:221], v[108:111]
	v_mfma_f32_16x16x32_bf16 v[100:103], v[178:181], v[218:221], v[100:103]
	v_mfma_f32_16x16x32_bf16 v[92:95], v[170:173], v[226:229], v[92:95]
	v_mfma_f32_16x16x32_bf16 v[84:87], v[178:181], v[226:229], v[84:87]
	s_setprio 0
	s_setprio 1
	v_mfma_f32_16x16x32_bf16 v[104:107], v[182:185], v[198:201], v[104:107]
	v_mfma_f32_16x16x32_bf16 v[96:99], v[190:193], v[198:201], v[96:99]
	v_mfma_f32_16x16x32_bf16 v[88:91], v[182:185], v[206:209], v[88:91]
	v_mfma_f32_16x16x32_bf16 v[80:83], v[190:193], v[206:209], v[80:83]
	v_mfma_f32_16x16x32_bf16 v[76:79], v[182:185], v[214:217], v[76:79]
	v_mfma_f32_16x16x32_bf16 v[72:75], v[190:193], v[214:217], v[72:75]
	v_mfma_f32_16x16x32_bf16 v[68:71], v[182:185], v[222:225], v[68:71]
	v_mfma_f32_16x16x32_bf16 v[64:67], v[190:193], v[222:225], v[64:67]
	v_mfma_f32_16x16x32_bf16 v[104:107], v[186:189], v[202:205], v[104:107]
	v_mfma_f32_16x16x32_bf16 v[96:99], v[194:197], v[202:205], v[96:99]
	v_mfma_f32_16x16x32_bf16 v[88:91], v[186:189], v[210:213], v[88:91]
	v_mfma_f32_16x16x32_bf16 v[80:83], v[194:197], v[210:213], v[80:83]
	v_mfma_f32_16x16x32_bf16 v[76:79], v[186:189], v[218:221], v[76:79]
	v_mfma_f32_16x16x32_bf16 v[72:75], v[194:197], v[218:221], v[72:75]
	v_mfma_f32_16x16x32_bf16 v[68:71], v[186:189], v[226:229], v[68:71]
	v_mfma_f32_16x16x32_bf16 v[64:67], v[194:197], v[226:229], v[64:67]
	s_setprio 0
	s_barrier
	s_add_i32 s63, s50, s1
	v_lshl_add_u64 v[232:233], s[44:45], 0, v[146:147]
	s_mov_b32 m0, s63
	ds_read_b128 v[198:201], v164 offset:16384
	ds_read_b128 v[202:205], v164 offset:17408
	ds_read_b128 v[206:209], v164 offset:18432
	ds_read_b128 v[210:213], v164 offset:19456
	ds_read_b128 v[214:217], v164 offset:20480
	ds_read_b128 v[218:221], v164 offset:21504
	ds_read_b128 v[222:225], v164 offset:22528
	ds_read_b128 v[226:229], v164 offset:23552
	global_load_lds_dwordx4 v[232:233], off
	s_add_i32 m0, s63, 0x2000
	s_add_u32 s64, s44, 0x80000
	v_lshl_add_u64 v[234:235], s[44:45], 0, v[148:149]
	s_addc_u32 s65, s45, 0
	s_add_i32 s63, s51, s1
	global_load_lds_dwordx4 v[234:235], off
	v_lshl_add_u64 v[236:237], s[64:65], 0, v[146:147]
	s_mov_b32 m0, s63
	v_mov_b32_e32 v231, v151
	global_load_lds_dwordx4 v[236:237], off
	v_lshl_add_u64 v[236:237], s[64:65], 0, v[148:149]
	s_add_i32 m0, s63, 0x2000
	s_nop 0
	global_load_lds_dwordx4 v[236:237], off
	s_mov_b32 m0, s4
	v_lshl_add_u64 v[236:237], s[46:47], 0, v[150:151]
	global_load_lds_dwordx4 v150, s[46:47]
	s_mov_b32 m0, s5
	s_nop 0
	global_load_lds_dwordx4 v230, s[46:47]
	s_waitcnt vmcnt(8)
	s_waitcnt lgkmcnt(0)
	v_lshl_add_u64 v[230:231], s[46:47], 0, v[230:231]
	s_barrier
	s_setprio 1
	v_mfma_f32_16x16x32_bf16 v[60:63], v[140:143], v[198:201], v[60:63]
	v_mfma_f32_16x16x32_bf16 v[56:59], v[174:177], v[198:201], v[56:59]
	v_mfma_f32_16x16x32_bf16 v[44:47], v[140:143], v[206:209], v[44:47]
	v_mfma_f32_16x16x32_bf16 v[36:39], v[174:177], v[206:209], v[36:39]
	v_mfma_f32_16x16x32_bf16 v[20:23], v[140:143], v[214:217], v[20:23]
	v_mfma_f32_16x16x32_bf16 v[12:15], v[174:177], v[214:217], v[12:15]
	v_mfma_f32_16x16x32_bf16 v[4:7], v[140:143], v[222:225], v[4:7]
	v_mfma_f32_16x16x32_bf16 v[0:3], v[174:177], v[222:225], v[0:3]
	v_mfma_f32_16x16x32_bf16 v[60:63], v[170:173], v[202:205], v[60:63]
	v_mfma_f32_16x16x32_bf16 v[56:59], v[178:181], v[202:205], v[56:59]
	v_mfma_f32_16x16x32_bf16 v[44:47], v[170:173], v[210:213], v[44:47]
	v_mfma_f32_16x16x32_bf16 v[36:39], v[178:181], v[210:213], v[36:39]
	v_mfma_f32_16x16x32_bf16 v[20:23], v[170:173], v[218:221], v[20:23]
	v_mfma_f32_16x16x32_bf16 v[12:15], v[178:181], v[218:221], v[12:15]
	v_mfma_f32_16x16x32_bf16 v[4:7], v[170:173], v[226:229], v[4:7]
	v_mfma_f32_16x16x32_bf16 v[0:3], v[178:181], v[226:229], v[0:3]
	s_setprio 0
	s_setprio 1
	v_mfma_f32_16x16x32_bf16 v[40:43], v[182:185], v[198:201], v[40:43]
	v_mfma_f32_16x16x32_bf16 v[32:35], v[190:193], v[198:201], v[32:35]
	v_mfma_f32_16x16x32_bf16 v[16:19], v[182:185], v[206:209], v[16:19]
	v_mfma_f32_16x16x32_bf16 v[8:11], v[190:193], v[206:209], v[8:11]
	v_mfma_f32_16x16x32_bf16 v[48:51], v[182:185], v[214:217], v[48:51]
	v_mfma_f32_16x16x32_bf16 v[52:55], v[190:193], v[214:217], v[52:55]
	v_mfma_f32_16x16x32_bf16 v[24:27], v[182:185], v[222:225], v[24:27]
	v_mfma_f32_16x16x32_bf16 v[28:31], v[190:193], v[222:225], v[28:31]
	v_mfma_f32_16x16x32_bf16 v[40:43], v[186:189], v[202:205], v[40:43]
	v_mfma_f32_16x16x32_bf16 v[32:35], v[194:197], v[202:205], v[32:35]
	v_mfma_f32_16x16x32_bf16 v[16:19], v[186:189], v[210:213], v[16:19]
	v_mfma_f32_16x16x32_bf16 v[8:11], v[194:197], v[210:213], v[8:11]
	v_mfma_f32_16x16x32_bf16 v[48:51], v[186:189], v[218:221], v[48:51]
	v_mfma_f32_16x16x32_bf16 v[52:55], v[194:197], v[218:221], v[52:55]
	v_mfma_f32_16x16x32_bf16 v[24:27], v[186:189], v[226:229], v[24:27]
	v_mfma_f32_16x16x32_bf16 v[28:31], v[194:197], v[226:229], v[28:31]
	s_setprio 0
	s_barrier
	s_add_i32 s63, 0, 0x18000
	v_add_u32_e32 v133, s63, v160
	s_add_i32 s64, 0, 0x1c000
	ds_read_b128 v[140:143], v133
	ds_read_b128 v[170:173], v133 offset:1024
	ds_read_b128 v[174:177], v133 offset:2048
	ds_read_b128 v[178:181], v133 offset:3072
	v_add_u32_e32 v133, s64, v160
	ds_read_b128 v[182:185], v133
	ds_read_b128 v[186:189], v133 offset:1024
	ds_read_b128 v[190:193], v133 offset:2048
	ds_read_b128 v[194:197], v133 offset:3072
	s_mov_b32 m0, s6
	ds_read_b128 v[198:201], v164 offset:32768
	ds_read_b128 v[202:205], v164 offset:33792
	ds_read_b128 v[206:209], v164 offset:34816
	ds_read_b128 v[210:213], v164 offset:35840
	ds_read_b128 v[214:217], v164 offset:36864
	ds_read_b128 v[218:221], v164 offset:37888
	ds_read_b128 v[222:225], v164 offset:38912
	ds_read_b128 v[226:229], v164 offset:39936
	global_load_lds_dwordx4 v129, s[46:47]
	s_mov_b32 m0, s7
	s_nop 0
	global_load_lds_dwordx4 v131, s[46:47]
	s_waitcnt vmcnt(8)
	s_waitcnt lgkmcnt(0)
	s_barrier
	s_setprio 1
	v_mfma_f32_16x16x32_bf16 v[124:127], v[140:143], v[198:201], v[124:127]
	v_mfma_f32_16x16x32_bf16 v[120:123], v[174:177], v[198:201], v[120:123]
	v_mfma_f32_16x16x32_bf16 v[116:119], v[140:143], v[206:209], v[116:119]
	v_mfma_f32_16x16x32_bf16 v[112:115], v[174:177], v[206:209], v[112:115]
	v_mfma_f32_16x16x32_bf16 v[108:111], v[140:143], v[214:217], v[108:111]
	v_mfma_f32_16x16x32_bf16 v[100:103], v[174:177], v[214:217], v[100:103]
	v_mfma_f32_16x16x32_bf16 v[92:95], v[140:143], v[222:225], v[92:95]
	v_mfma_f32_16x16x32_bf16 v[84:87], v[174:177], v[222:225], v[84:87]
	v_mfma_f32_16x16x32_bf16 v[124:127], v[170:173], v[202:205], v[124:127]
	v_mfma_f32_16x16x32_bf16 v[120:123], v[178:181], v[202:205], v[120:123]
	v_mfma_f32_16x16x32_bf16 v[116:119], v[170:173], v[210:213], v[116:119]
	v_mfma_f32_16x16x32_bf16 v[112:115], v[178:181], v[210:213], v[112:115]
	v_mfma_f32_16x16x32_bf16 v[108:111], v[170:173], v[218:221], v[108:111]
	v_mfma_f32_16x16x32_bf16 v[100:103], v[178:181], v[218:221], v[100:103]
	v_mfma_f32_16x16x32_bf16 v[92:95], v[170:173], v[226:229], v[92:95]
	v_mfma_f32_16x16x32_bf16 v[84:87], v[178:181], v[226:229], v[84:87]
	s_setprio 0
	s_setprio 1
	v_mfma_f32_16x16x32_bf16 v[104:107], v[182:185], v[198:201], v[104:107]
	v_mfma_f32_16x16x32_bf16 v[96:99], v[190:193], v[198:201], v[96:99]
	v_mfma_f32_16x16x32_bf16 v[88:91], v[182:185], v[206:209], v[88:91]
	v_mfma_f32_16x16x32_bf16 v[80:83], v[190:193], v[206:209], v[80:83]
	v_mfma_f32_16x16x32_bf16 v[76:79], v[182:185], v[214:217], v[76:79]
	v_mfma_f32_16x16x32_bf16 v[72:75], v[190:193], v[214:217], v[72:75]
	v_mfma_f32_16x16x32_bf16 v[68:71], v[182:185], v[222:225], v[68:71]
	v_mfma_f32_16x16x32_bf16 v[64:67], v[190:193], v[222:225], v[64:67]
	v_mfma_f32_16x16x32_bf16 v[104:107], v[186:189], v[202:205], v[104:107]
	v_mfma_f32_16x16x32_bf16 v[96:99], v[194:197], v[202:205], v[96:99]
	v_mfma_f32_16x16x32_bf16 v[88:91], v[186:189], v[210:213], v[88:91]
	v_mfma_f32_16x16x32_bf16 v[80:83], v[194:197], v[210:213], v[80:83]
	v_mfma_f32_16x16x32_bf16 v[76:79], v[186:189], v[218:221], v[76:79]
	v_mfma_f32_16x16x32_bf16 v[72:75], v[194:197], v[218:221], v[72:75]
	v_mfma_f32_16x16x32_bf16 v[68:71], v[186:189], v[226:229], v[68:71]
	v_mfma_f32_16x16x32_bf16 v[64:67], v[194:197], v[226:229], v[64:67]
	s_setprio 0
	s_barrier
	s_add_i32 s46, s63, s1
	v_lshl_add_u64 v[232:233], v[232:233], 0, s[24:25]
	s_mov_b32 m0, s46
	ds_read_b128 v[198:201], v164 offset:49152
	ds_read_b128 v[202:205], v164 offset:50176
	ds_read_b128 v[206:209], v164 offset:51200
	ds_read_b128 v[210:213], v164 offset:52224
	ds_read_b128 v[214:217], v164 offset:53248
	ds_read_b128 v[218:221], v164 offset:54272
	ds_read_b128 v[222:225], v164 offset:55296
	ds_read_b128 v[226:229], v164 offset:56320
	global_load_lds_dwordx4 v[232:233], off
	s_add_i32 m0, s46, 0x2000
	s_add_u32 s44, s44, 0x80080
	v_lshl_add_u64 v[232:233], v[234:235], 0, s[24:25]
	s_addc_u32 s45, s45, 0
	s_add_i32 s46, s64, s1
	global_load_lds_dwordx4 v[232:233], off
	v_lshl_add_u64 v[232:233], s[44:45], 0, v[146:147]
	s_mov_b32 m0, s46
	v_lshl_add_u64 v[230:231], v[230:231], 0, s[24:25]
	global_load_lds_dwordx4 v[232:233], off
	v_lshl_add_u64 v[232:233], s[44:45], 0, v[148:149]
	s_add_i32 m0, s46, 0x2000
	s_nop 0
	global_load_lds_dwordx4 v[232:233], off
	v_lshl_add_u64 v[232:233], v[236:237], 0, s[24:25]
	s_mov_b32 m0, s9
	s_nop 0
	global_load_lds_dwordx4 v[232:233], off
	s_mov_b32 m0, s48
	s_nop 0
	global_load_lds_dwordx4 v[230:231], off
	s_waitcnt vmcnt(8)
	s_waitcnt lgkmcnt(0)
	s_barrier
	s_setprio 1
	v_mfma_f32_16x16x32_bf16 v[60:63], v[140:143], v[198:201], v[60:63]
	v_mfma_f32_16x16x32_bf16 v[56:59], v[174:177], v[198:201], v[56:59]
	v_mfma_f32_16x16x32_bf16 v[44:47], v[140:143], v[206:209], v[44:47]
	v_mfma_f32_16x16x32_bf16 v[36:39], v[174:177], v[206:209], v[36:39]
	v_mfma_f32_16x16x32_bf16 v[20:23], v[140:143], v[214:217], v[20:23]
	v_mfma_f32_16x16x32_bf16 v[12:15], v[174:177], v[214:217], v[12:15]
	v_mfma_f32_16x16x32_bf16 v[4:7], v[140:143], v[222:225], v[4:7]
	v_mfma_f32_16x16x32_bf16 v[0:3], v[174:177], v[222:225], v[0:3]
	v_mfma_f32_16x16x32_bf16 v[60:63], v[170:173], v[202:205], v[60:63]
	v_mfma_f32_16x16x32_bf16 v[56:59], v[178:181], v[202:205], v[56:59]
	v_mfma_f32_16x16x32_bf16 v[44:47], v[170:173], v[210:213], v[44:47]
	v_mfma_f32_16x16x32_bf16 v[36:39], v[178:181], v[210:213], v[36:39]
	v_mfma_f32_16x16x32_bf16 v[20:23], v[170:173], v[218:221], v[20:23]
	v_mfma_f32_16x16x32_bf16 v[12:15], v[178:181], v[218:221], v[12:15]
	v_mfma_f32_16x16x32_bf16 v[4:7], v[170:173], v[226:229], v[4:7]
	v_mfma_f32_16x16x32_bf16 v[0:3], v[178:181], v[226:229], v[0:3]
	s_setprio 0
	s_setprio 1
	v_mfma_f32_16x16x32_bf16 v[40:43], v[182:185], v[198:201], v[40:43]
	v_mfma_f32_16x16x32_bf16 v[32:35], v[190:193], v[198:201], v[32:35]
	v_mfma_f32_16x16x32_bf16 v[16:19], v[182:185], v[206:209], v[16:19]
	v_mfma_f32_16x16x32_bf16 v[8:11], v[190:193], v[206:209], v[8:11]
	v_mfma_f32_16x16x32_bf16 v[48:51], v[182:185], v[214:217], v[48:51]
	v_mfma_f32_16x16x32_bf16 v[52:55], v[190:193], v[214:217], v[52:55]
	v_mfma_f32_16x16x32_bf16 v[24:27], v[182:185], v[222:225], v[24:27]
	v_mfma_f32_16x16x32_bf16 v[28:31], v[190:193], v[222:225], v[28:31]
	v_mfma_f32_16x16x32_bf16 v[40:43], v[186:189], v[202:205], v[40:43]
	v_mfma_f32_16x16x32_bf16 v[32:35], v[194:197], v[202:205], v[32:35]
	v_mfma_f32_16x16x32_bf16 v[16:19], v[186:189], v[210:213], v[16:19]
	v_mfma_f32_16x16x32_bf16 v[8:11], v[194:197], v[210:213], v[8:11]
	v_mfma_f32_16x16x32_bf16 v[48:51], v[186:189], v[218:221], v[48:51]
	v_mfma_f32_16x16x32_bf16 v[52:55], v[194:197], v[218:221], v[52:55]
	v_mfma_f32_16x16x32_bf16 v[24:27], v[186:189], v[226:229], v[24:27]
	v_mfma_f32_16x16x32_bf16 v[28:31], v[194:197], v[226:229], v[28:31]
	s_setprio 0
	s_add_i32 s62, s62, 2
	s_add_u32 s12, s12, 0x100
	s_addc_u32 s13, s13, 0
	s_cmp_gt_u32 s62, 29
	s_barrier
	s_cbranch_scc0 .LBB0_964
	s_and_b64 vcc, exec, s[26:27]
	s_cbranch_vccz .LBB0_967
	s_barrier

.LBB0_1359:
	v_add_u32_e32 v165, s51, v143
	ds_read_b128 v[166:169], v165
	ds_read_b128 v[170:173], v165 offset:1024
	ds_read_b128 v[174:177], v165 offset:2048
	ds_read_b128 v[178:181], v165 offset:3072
	v_add_u32_e32 v165, s52, v143
	ds_read_b128 v[182:185], v165
	ds_read_b128 v[186:189], v165 offset:1024
	ds_read_b128 v[190:193], v165 offset:2048
	ds_read_b128 v[194:197], v165 offset:3072
	s_cmpk_eq_i32 s14, 0x1000
	s_cselect_b64 vcc, -1, 0
	s_and_b64 s[48:49], vcc, exec
	s_cselect_b32 s48, 0, s14
	v_lshl_add_u64 v[154:155], v[148:149], 0, s[14:15]
	s_cselect_b32 s49, 0, s15
	s_add_u32 s48, s22, s48
	v_cndmask_b32_e32 v132, v146, v160, vcc
	v_cndmask_b32_e32 v139, v140, v162, vcc
	v_cndmask_b32_e32 v230, v142, v161, vcc
	v_cndmask_b32_e32 v141, v138, v163, vcc
	v_cndmask_b32_e32 v154, v154, v164, vcc
	v_cndmask_b32_e32 v155, v155, v135, vcc
	s_addc_u32 s49, s23, s49
	v_lshl_add_u64 v[232:233], v[152:153], 0, s[14:15]
	s_mov_b32 m0, s53
	v_lshl_add_u64 v[232:233], v[232:233], 0, s[42:43]
	ds_read_b128 v[198:201], v159
	ds_read_b128 v[202:205], v159 offset:1024
	ds_read_b128 v[206:209], v159 offset:2048
	ds_read_b128 v[210:213], v159 offset:3072
	ds_read_b128 v[214:217], v159 offset:4096
	ds_read_b128 v[218:221], v159 offset:5120
	ds_read_b128 v[222:225], v159 offset:6144
	ds_read_b128 v[226:229], v159 offset:7168
	global_load_lds_dwordx4 v[232:233], off
	v_lshl_add_u64 v[232:233], v[150:151], 0, s[14:15]
	v_lshl_add_u64 v[232:233], v[232:233], 0, s[42:43]
	s_mov_b32 m0, s55
	s_nop 0
	global_load_lds_dwordx4 v[232:233], off
	s_waitcnt vmcnt(8)
	s_waitcnt lgkmcnt(0)
	s_barrier
	s_setprio 1
	v_mfma_f32_16x16x32_bf16 v[124:127], v[166:169], v[198:201], v[124:127]
	v_mfma_f32_16x16x32_bf16 v[120:123], v[174:177], v[198:201], v[120:123]
	v_mfma_f32_16x16x32_bf16 v[108:111], v[166:169], v[206:209], v[108:111]
	v_mfma_f32_16x16x32_bf16 v[104:107], v[174:177], v[206:209], v[104:107]
	v_mfma_f32_16x16x32_bf16 v[92:95], v[166:169], v[214:217], v[92:95]
	v_mfma_f32_16x16x32_bf16 v[88:91], v[174:177], v[214:217], v[88:91]
	v_mfma_f32_16x16x32_bf16 v[76:79], v[166:169], v[222:225], v[76:79]
	v_mfma_f32_16x16x32_bf16 v[72:75], v[174:177], v[222:225], v[72:75]
	v_mfma_f32_16x16x32_bf16 v[124:127], v[170:173], v[202:205], v[124:127]
	v_mfma_f32_16x16x32_bf16 v[120:123], v[178:181], v[202:205], v[120:123]
	v_mfma_f32_16x16x32_bf16 v[108:111], v[170:173], v[210:213], v[108:111]
	v_mfma_f32_16x16x32_bf16 v[104:107], v[178:181], v[210:213], v[104:107]
	v_mfma_f32_16x16x32_bf16 v[92:95], v[170:173], v[218:221], v[92:95]
	v_mfma_f32_16x16x32_bf16 v[88:91], v[178:181], v[218:221], v[88:91]
	v_mfma_f32_16x16x32_bf16 v[76:79], v[170:173], v[226:229], v[76:79]
	v_mfma_f32_16x16x32_bf16 v[72:75], v[178:181], v[226:229], v[72:75]
	s_setprio 0
	s_setprio 1
	v_mfma_f32_16x16x32_bf16 v[116:119], v[182:185], v[198:201], v[116:119]
	v_mfma_f32_16x16x32_bf16 v[112:115], v[190:193], v[198:201], v[112:115]
	v_mfma_f32_16x16x32_bf16 v[100:103], v[182:185], v[206:209], v[100:103]
	v_mfma_f32_16x16x32_bf16 v[96:99], v[190:193], v[206:209], v[96:99]
	v_mfma_f32_16x16x32_bf16 v[84:87], v[182:185], v[214:217], v[84:87]
	v_mfma_f32_16x16x32_bf16 v[80:83], v[190:193], v[214:217], v[80:83]
	v_mfma_f32_16x16x32_bf16 v[68:71], v[182:185], v[222:225], v[68:71]
	v_mfma_f32_16x16x32_bf16 v[64:67], v[190:193], v[222:225], v[64:67]
	v_mfma_f32_16x16x32_bf16 v[116:119], v[186:189], v[202:205], v[116:119]
	v_mfma_f32_16x16x32_bf16 v[112:115], v[194:197], v[202:205], v[112:115]
	v_mfma_f32_16x16x32_bf16 v[100:103], v[186:189], v[210:213], v[100:103]
	v_mfma_f32_16x16x32_bf16 v[96:99], v[194:197], v[210:213], v[96:99]
	v_mfma_f32_16x16x32_bf16 v[84:87], v[186:189], v[218:221], v[84:87]
	v_mfma_f32_16x16x32_bf16 v[80:83], v[194:197], v[218:221], v[80:83]
	v_mfma_f32_16x16x32_bf16 v[68:71], v[186:189], v[226:229], v[68:71]
	v_mfma_f32_16x16x32_bf16 v[64:67], v[194:197], v[226:229], v[64:67]
	s_setprio 0
	s_barrier
	s_mov_b32 m0, s57
	v_lshl_add_u64 v[232:233], v[154:155], 0, v[128:129]
	ds_read_b128 v[198:201], v159 offset:16384
	ds_read_b128 v[202:205], v159 offset:17408
	ds_read_b128 v[206:209], v159 offset:18432
	ds_read_b128 v[210:213], v159 offset:19456
	ds_read_b128 v[214:217], v159 offset:20480
	ds_read_b128 v[218:221], v159 offset:21504
	ds_read_b128 v[222:225], v159 offset:22528
	ds_read_b128 v[226:229], v159 offset:23552
	global_load_lds_dwordx4 v[232:233], off
	v_lshl_add_u64 v[234:235], v[154:155], 0, v[130:131]
	s_mov_b32 m0, s59
	v_lshl_add_u64 v[236:237], v[154:155], 0, s[30:31]
	global_load_lds_dwordx4 v[234:235], off
	v_lshl_add_u64 v[238:239], v[236:237], 0, v[128:129]
	s_mov_b32 m0, s60
	v_lshl_add_u64 v[236:237], v[236:237], 0, v[130:131]
	global_load_lds_dwordx4 v[238:239], off
	s_mov_b32 m0, s61
	v_mov_b32_e32 v231, v133
	global_load_lds_dwordx4 v[236:237], off
	s_mov_b32 m0, s1
	v_lshl_add_u64 v[236:237], s[48:49], 0, v[132:133]
	global_load_lds_dwordx4 v132, s[48:49]
	s_mov_b32 m0, s4
	s_nop 0
	global_load_lds_dwordx4 v230, s[48:49]
	s_waitcnt vmcnt(8)
	s_waitcnt lgkmcnt(0)
	v_lshl_add_u64 v[230:231], s[48:49], 0, v[230:231]
	s_barrier
	s_setprio 1
	v_mfma_f32_16x16x32_bf16 v[60:63], v[166:169], v[198:201], v[60:63]
	v_mfma_f32_16x16x32_bf16 v[56:59], v[174:177], v[198:201], v[56:59]
	v_mfma_f32_16x16x32_bf16 v[44:47], v[166:169], v[206:209], v[44:47]
	v_mfma_f32_16x16x32_bf16 v[36:39], v[174:177], v[206:209], v[36:39]
	v_mfma_f32_16x16x32_bf16 v[20:23], v[166:169], v[214:217], v[20:23]
	v_mfma_f32_16x16x32_bf16 v[8:11], v[174:177], v[214:217], v[8:11]
	v_mfma_f32_16x16x32_bf16 v[4:7], v[166:169], v[222:225], v[4:7]
	v_mfma_f32_16x16x32_bf16 v[0:3], v[174:177], v[222:225], v[0:3]
	v_mfma_f32_16x16x32_bf16 v[60:63], v[170:173], v[202:205], v[60:63]
	v_mfma_f32_16x16x32_bf16 v[56:59], v[178:181], v[202:205], v[56:59]
	v_mfma_f32_16x16x32_bf16 v[44:47], v[170:173], v[210:213], v[44:47]
	v_mfma_f32_16x16x32_bf16 v[36:39], v[178:181], v[210:213], v[36:39]
	v_mfma_f32_16x16x32_bf16 v[20:23], v[170:173], v[218:221], v[20:23]
	v_mfma_f32_16x16x32_bf16 v[8:11], v[178:181], v[218:221], v[8:11]
	v_mfma_f32_16x16x32_bf16 v[4:7], v[170:173], v[226:229], v[4:7]
	v_mfma_f32_16x16x32_bf16 v[0:3], v[178:181], v[226:229], v[0:3]
	s_setprio 0
	s_setprio 1
	v_mfma_f32_16x16x32_bf16 v[52:55], v[182:185], v[198:201], v[52:55]
	v_mfma_f32_16x16x32_bf16 v[48:51], v[190:193], v[198:201], v[48:51]
	v_mfma_f32_16x16x32_bf16 v[28:31], v[182:185], v[206:209], v[28:31]
	v_mfma_f32_16x16x32_bf16 v[24:27], v[190:193], v[206:209], v[24:27]
	v_mfma_f32_16x16x32_bf16 v[40:43], v[182:185], v[214:217], v[40:43]
	v_mfma_f32_16x16x32_bf16 v[32:35], v[190:193], v[214:217], v[32:35]
	v_mfma_f32_16x16x32_bf16 v[16:19], v[182:185], v[222:225], v[16:19]
	v_mfma_f32_16x16x32_bf16 v[12:15], v[190:193], v[222:225], v[12:15]
	v_mfma_f32_16x16x32_bf16 v[52:55], v[186:189], v[202:205], v[52:55]
	v_mfma_f32_16x16x32_bf16 v[48:51], v[194:197], v[202:205], v[48:51]
	v_mfma_f32_16x16x32_bf16 v[28:31], v[186:189], v[210:213], v[28:31]
	v_mfma_f32_16x16x32_bf16 v[24:27], v[194:197], v[210:213], v[24:27]
	v_mfma_f32_16x16x32_bf16 v[40:43], v[186:189], v[218:221], v[40:43]
	v_mfma_f32_16x16x32_bf16 v[32:35], v[194:197], v[218:221], v[32:35]
	v_mfma_f32_16x16x32_bf16 v[16:19], v[186:189], v[226:229], v[16:19]
	v_mfma_f32_16x16x32_bf16 v[12:15], v[194:197], v[226:229], v[12:15]
	s_setprio 0
	s_barrier
	v_add_u32_e32 v132, s62, v143
	ds_read_b128 v[166:169], v132
	ds_read_b128 v[170:173], v132 offset:1024
	ds_read_b128 v[174:177], v132 offset:2048
	ds_read_b128 v[178:181], v132 offset:3072
	v_add_u32_e32 v132, s63, v143
	ds_read_b128 v[182:185], v132
	ds_read_b128 v[186:189], v132 offset:1024
	ds_read_b128 v[190:193], v132 offset:2048
	ds_read_b128 v[194:197], v132 offset:3072
	s_mov_b32 m0, s5
	ds_read_b128 v[198:201], v159 offset:32768
	ds_read_b128 v[202:205], v159 offset:33792
	ds_read_b128 v[206:209], v159 offset:34816
	ds_read_b128 v[210:213], v159 offset:35840
	ds_read_b128 v[214:217], v159 offset:36864
	ds_read_b128 v[218:221], v159 offset:37888
	ds_read_b128 v[222:225], v159 offset:38912
	ds_read_b128 v[226:229], v159 offset:39936
	global_load_lds_dwordx4 v139, s[48:49]
	s_mov_b32 m0, s6
	s_nop 0
	global_load_lds_dwordx4 v141, s[48:49]
	s_waitcnt vmcnt(8)
	s_waitcnt lgkmcnt(0)
	s_barrier
	s_setprio 1
	v_mfma_f32_16x16x32_bf16 v[124:127], v[166:169], v[198:201], v[124:127]
	v_mfma_f32_16x16x32_bf16 v[120:123], v[174:177], v[198:201], v[120:123]
	v_mfma_f32_16x16x32_bf16 v[108:111], v[166:169], v[206:209], v[108:111]
	v_mfma_f32_16x16x32_bf16 v[104:107], v[174:177], v[206:209], v[104:107]
	v_mfma_f32_16x16x32_bf16 v[92:95], v[166:169], v[214:217], v[92:95]
	v_mfma_f32_16x16x32_bf16 v[88:91], v[174:177], v[214:217], v[88:91]
	v_mfma_f32_16x16x32_bf16 v[76:79], v[166:169], v[222:225], v[76:79]
	v_mfma_f32_16x16x32_bf16 v[72:75], v[174:177], v[222:225], v[72:75]
	v_mfma_f32_16x16x32_bf16 v[124:127], v[170:173], v[202:205], v[124:127]
	v_mfma_f32_16x16x32_bf16 v[120:123], v[178:181], v[202:205], v[120:123]
	v_mfma_f32_16x16x32_bf16 v[108:111], v[170:173], v[210:213], v[108:111]
	v_mfma_f32_16x16x32_bf16 v[104:107], v[178:181], v[210:213], v[104:107]
	v_mfma_f32_16x16x32_bf16 v[92:95], v[170:173], v[218:221], v[92:95]
	v_mfma_f32_16x16x32_bf16 v[88:91], v[178:181], v[218:221], v[88:91]
	v_mfma_f32_16x16x32_bf16 v[76:79], v[170:173], v[226:229], v[76:79]
	v_mfma_f32_16x16x32_bf16 v[72:75], v[178:181], v[226:229], v[72:75]
	s_setprio 0
	s_setprio 1
	v_mfma_f32_16x16x32_bf16 v[116:119], v[182:185], v[198:201], v[116:119]
	v_mfma_f32_16x16x32_bf16 v[112:115], v[190:193], v[198:201], v[112:115]
	v_mfma_f32_16x16x32_bf16 v[100:103], v[182:185], v[206:209], v[100:103]
	v_mfma_f32_16x16x32_bf16 v[96:99], v[190:193], v[206:209], v[96:99]
	v_mfma_f32_16x16x32_bf16 v[84:87], v[182:185], v[214:217], v[84:87]
	v_mfma_f32_16x16x32_bf16 v[80:83], v[190:193], v[214:217], v[80:83]
	v_mfma_f32_16x16x32_bf16 v[68:71], v[182:185], v[222:225], v[68:71]
	v_mfma_f32_16x16x32_bf16 v[64:67], v[190:193], v[222:225], v[64:67]
	v_mfma_f32_16x16x32_bf16 v[116:119], v[186:189], v[202:205], v[116:119]
	v_mfma_f32_16x16x32_bf16 v[112:115], v[194:197], v[202:205], v[112:115]
	v_mfma_f32_16x16x32_bf16 v[100:103], v[186:189], v[210:213], v[100:103]
	v_mfma_f32_16x16x32_bf16 v[96:99], v[194:197], v[210:213], v[96:99]
	v_mfma_f32_16x16x32_bf16 v[84:87], v[186:189], v[218:221], v[84:87]
	v_mfma_f32_16x16x32_bf16 v[80:83], v[194:197], v[218:221], v[80:83]
	v_mfma_f32_16x16x32_bf16 v[68:71], v[186:189], v[226:229], v[68:71]
	v_mfma_f32_16x16x32_bf16 v[64:67], v[194:197], v[226:229], v[64:67]
	s_setprio 0
	s_barrier
	s_add_i32 s48, s62, s0
	v_lshl_add_u64 v[232:233], v[232:233], 0, s[36:37]
	s_mov_b32 m0, s48
	ds_read_b128 v[198:201], v159 offset:49152
	ds_read_b128 v[202:205], v159 offset:50176
	ds_read_b128 v[206:209], v159 offset:51200
	ds_read_b128 v[210:213], v159 offset:52224
	ds_read_b128 v[214:217], v159 offset:53248
	ds_read_b128 v[218:221], v159 offset:54272
	ds_read_b128 v[222:225], v159 offset:55296
	ds_read_b128 v[226:229], v159 offset:56320
	global_load_lds_dwordx4 v[232:233], off
	v_lshl_add_u64 v[232:233], v[234:235], 0, s[36:37]
	s_add_i32 m0, s48, 0x2000
	v_lshl_add_u64 v[154:155], v[154:155], 0, s[38:39]
	s_add_i32 s48, s63, s0
	global_load_lds_dwordx4 v[232:233], off
	v_lshl_add_u64 v[232:233], v[154:155], 0, v[128:129]
	s_mov_b32 m0, s48
	v_lshl_add_u64 v[154:155], v[154:155], 0, v[130:131]
	global_load_lds_dwordx4 v[232:233], off
	s_add_i32 m0, s48, 0x2000
	s_nop 0
	global_load_lds_dwordx4 v[154:155], off
	v_lshl_add_u64 v[154:155], v[236:237], 0, s[36:37]
	s_mov_b32 m0, s9
	s_nop 0
	global_load_lds_dwordx4 v[154:155], off
	v_lshl_add_u64 v[154:155], v[230:231], 0, s[36:37]
	s_mov_b32 m0, s28
	s_nop 0
	global_load_lds_dwordx4 v[154:155], off
	s_waitcnt vmcnt(8)
	s_waitcnt lgkmcnt(0)
	s_barrier
	s_setprio 1
	v_mfma_f32_16x16x32_bf16 v[60:63], v[166:169], v[198:201], v[60:63]
	v_mfma_f32_16x16x32_bf16 v[56:59], v[174:177], v[198:201], v[56:59]
	v_mfma_f32_16x16x32_bf16 v[44:47], v[166:169], v[206:209], v[44:47]
	v_mfma_f32_16x16x32_bf16 v[36:39], v[174:177], v[206:209], v[36:39]
	v_mfma_f32_16x16x32_bf16 v[20:23], v[166:169], v[214:217], v[20:23]
	v_mfma_f32_16x16x32_bf16 v[8:11], v[174:177], v[214:217], v[8:11]
	v_mfma_f32_16x16x32_bf16 v[4:7], v[166:169], v[222:225], v[4:7]
	v_mfma_f32_16x16x32_bf16 v[0:3], v[174:177], v[222:225], v[0:3]
	v_mfma_f32_16x16x32_bf16 v[60:63], v[170:173], v[202:205], v[60:63]
	v_mfma_f32_16x16x32_bf16 v[56:59], v[178:181], v[202:205], v[56:59]
	v_mfma_f32_16x16x32_bf16 v[44:47], v[170:173], v[210:213], v[44:47]
	v_mfma_f32_16x16x32_bf16 v[36:39], v[178:181], v[210:213], v[36:39]
	v_mfma_f32_16x16x32_bf16 v[20:23], v[170:173], v[218:221], v[20:23]
	v_mfma_f32_16x16x32_bf16 v[8:11], v[178:181], v[218:221], v[8:11]
	v_mfma_f32_16x16x32_bf16 v[4:7], v[170:173], v[226:229], v[4:7]
	v_mfma_f32_16x16x32_bf16 v[0:3], v[178:181], v[226:229], v[0:3]
	s_setprio 0
	s_setprio 1
	v_mfma_f32_16x16x32_bf16 v[52:55], v[182:185], v[198:201], v[52:55]
	v_mfma_f32_16x16x32_bf16 v[48:51], v[190:193], v[198:201], v[48:51]
	v_mfma_f32_16x16x32_bf16 v[28:31], v[182:185], v[206:209], v[28:31]
	v_mfma_f32_16x16x32_bf16 v[24:27], v[190:193], v[206:209], v[24:27]
	v_mfma_f32_16x16x32_bf16 v[40:43], v[182:185], v[214:217], v[40:43]
	v_mfma_f32_16x16x32_bf16 v[32:35], v[190:193], v[214:217], v[32:35]
	v_mfma_f32_16x16x32_bf16 v[16:19], v[182:185], v[222:225], v[16:19]
	v_mfma_f32_16x16x32_bf16 v[12:15], v[190:193], v[222:225], v[12:15]
	v_mfma_f32_16x16x32_bf16 v[52:55], v[186:189], v[202:205], v[52:55]
	v_mfma_f32_16x16x32_bf16 v[48:51], v[194:197], v[202:205], v[48:51]
	v_mfma_f32_16x16x32_bf16 v[28:31], v[186:189], v[210:213], v[28:31]
	v_mfma_f32_16x16x32_bf16 v[24:27], v[194:197], v[210:213], v[24:27]
	v_mfma_f32_16x16x32_bf16 v[40:43], v[186:189], v[218:221], v[40:43]
	v_mfma_f32_16x16x32_bf16 v[32:35], v[194:197], v[218:221], v[32:35]
	v_mfma_f32_16x16x32_bf16 v[16:19], v[186:189], v[226:229], v[16:19]
	v_mfma_f32_16x16x32_bf16 v[12:15], v[194:197], v[226:229], v[12:15]
	s_setprio 0
	s_add_i32 s47, s47, 2
	s_add_u32 s14, s14, 0x100
	s_addc_u32 s15, s15, 0
	s_cmp_gt_u32 s47, 29
	s_barrier
	s_cbranch_scc0 .LBB0_1359
	s_and_b64 vcc, exec, s[40:41]
	s_cbranch_vccz .LBB0_1362
	s_barrier

.LBB0_1571:
	ds_read_b128 v[170:173], v163
	ds_read_b128 v[174:177], v163 offset:1024
	ds_read_b128 v[178:181], v163 offset:2048
	ds_read_b128 v[182:185], v163 offset:3072
	ds_read_b128 v[186:189], v164
	ds_read_b128 v[190:193], v164 offset:1024
	ds_read_b128 v[194:197], v164 offset:2048
	ds_read_b128 v[198:201], v164 offset:3072
	s_add_u32 s46, s42, s10
	s_addc_u32 s47, s43, s11
	s_cmpk_eq_i32 s10, 0x1000
	s_cselect_b64 vcc, -1, 0
	s_and_b64 s[44:45], vcc, exec
	s_cselect_b32 s64, 0, s10
	s_cselect_b32 s63, 0, s11
	s_cselect_b32 s44, s39, s46
	s_cselect_b32 s45, s13, s47
	s_add_u32 s46, s20, s64
	v_cndmask_b32_e32 v140, v128, v166, vcc
	v_cndmask_b32_e32 v129, v132, v168, vcc
	v_cndmask_b32_e32 v154, v130, v167, vcc
	v_cndmask_b32_e32 v131, v134, v169, vcc
	s_addc_u32 s47, s21, s63
	v_lshl_add_u64 v[234:235], v[152:153], 0, s[10:11]
	v_lshl_add_u64 v[234:235], v[234:235], 0, s[18:19]
	s_add_i32 m0, s5, 0xc000
	ds_read_b128 v[202:205], v165
	ds_read_b128 v[206:209], v165 offset:1024
	ds_read_b128 v[210:213], v165 offset:2048
	ds_read_b128 v[214:217], v165 offset:3072
	ds_read_b128 v[218:221], v165 offset:4096
	ds_read_b128 v[222:225], v165 offset:5120
	ds_read_b128 v[226:229], v165 offset:6144
	ds_read_b128 v[230:233], v165 offset:7168
	global_load_lds_dwordx4 v[234:235], off
	v_lshl_add_u64 v[234:235], v[150:151], 0, s[10:11]
	v_lshl_add_u64 v[234:235], v[234:235], 0, s[18:19]
	s_add_i32 m0, s5, 0xe000
	s_nop 0
	global_load_lds_dwordx4 v[234:235], off
	s_waitcnt vmcnt(8)
	s_waitcnt lgkmcnt(0)
	s_barrier
	s_setprio 1
	v_mfma_f32_16x16x32_bf16 v[60:63], v[170:173], v[202:205], v[60:63]
	v_mfma_f32_16x16x32_bf16 v[56:59], v[178:181], v[202:205], v[56:59]
	v_mfma_f32_16x16x32_bf16 v[52:55], v[170:173], v[210:213], v[52:55]
	v_mfma_f32_16x16x32_bf16 v[48:51], v[178:181], v[210:213], v[48:51]
	v_mfma_f32_16x16x32_bf16 v[44:47], v[170:173], v[218:221], v[44:47]
	v_mfma_f32_16x16x32_bf16 v[40:43], v[178:181], v[218:221], v[40:43]
	v_mfma_f32_16x16x32_bf16 v[36:39], v[170:173], v[226:229], v[36:39]
	v_mfma_f32_16x16x32_bf16 v[32:35], v[178:181], v[226:229], v[32:35]
	v_mfma_f32_16x16x32_bf16 v[60:63], v[174:177], v[206:209], v[60:63]
	v_mfma_f32_16x16x32_bf16 v[56:59], v[182:185], v[206:209], v[56:59]
	v_mfma_f32_16x16x32_bf16 v[52:55], v[174:177], v[214:217], v[52:55]
	v_mfma_f32_16x16x32_bf16 v[48:51], v[182:185], v[214:217], v[48:51]
	v_mfma_f32_16x16x32_bf16 v[44:47], v[174:177], v[222:225], v[44:47]
	v_mfma_f32_16x16x32_bf16 v[40:43], v[182:185], v[222:225], v[40:43]
	v_mfma_f32_16x16x32_bf16 v[36:39], v[174:177], v[230:233], v[36:39]
	v_mfma_f32_16x16x32_bf16 v[32:35], v[182:185], v[230:233], v[32:35]
	s_setprio 0
	s_setprio 1
	v_mfma_f32_16x16x32_bf16 v[124:127], v[186:189], v[202:205], v[124:127]
	v_mfma_f32_16x16x32_bf16 v[120:123], v[194:197], v[202:205], v[120:123]
	v_mfma_f32_16x16x32_bf16 v[116:119], v[186:189], v[210:213], v[116:119]
	v_mfma_f32_16x16x32_bf16 v[112:115], v[194:197], v[210:213], v[112:115]
	v_mfma_f32_16x16x32_bf16 v[108:111], v[186:189], v[218:221], v[108:111]
	v_mfma_f32_16x16x32_bf16 v[104:107], v[194:197], v[218:221], v[104:107]
	v_mfma_f32_16x16x32_bf16 v[100:103], v[186:189], v[226:229], v[100:103]
	v_mfma_f32_16x16x32_bf16 v[96:99], v[194:197], v[226:229], v[96:99]
	v_mfma_f32_16x16x32_bf16 v[124:127], v[190:193], v[206:209], v[124:127]
	v_mfma_f32_16x16x32_bf16 v[120:123], v[198:201], v[206:209], v[120:123]
	v_mfma_f32_16x16x32_bf16 v[116:119], v[190:193], v[214:217], v[116:119]
	v_mfma_f32_16x16x32_bf16 v[112:115], v[198:201], v[214:217], v[112:115]
	v_mfma_f32_16x16x32_bf16 v[108:111], v[190:193], v[222:225], v[108:111]
	v_mfma_f32_16x16x32_bf16 v[104:107], v[198:201], v[222:225], v[104:107]
	v_mfma_f32_16x16x32_bf16 v[100:103], v[190:193], v[230:233], v[100:103]
	v_mfma_f32_16x16x32_bf16 v[96:99], v[198:201], v[230:233], v[96:99]
	s_setprio 0
	s_barrier
	s_add_i32 s63, s55, s0
	v_lshl_add_u64 v[234:235], s[44:45], 0, v[136:137]
	s_mov_b32 m0, s63
	ds_read_b128 v[202:205], v165 offset:16384
	ds_read_b128 v[206:209], v165 offset:17408
	ds_read_b128 v[210:213], v165 offset:18432
	ds_read_b128 v[214:217], v165 offset:19456
	ds_read_b128 v[218:221], v165 offset:20480
	ds_read_b128 v[222:225], v165 offset:21504
	ds_read_b128 v[226:229], v165 offset:22528
	ds_read_b128 v[230:233], v165 offset:23552
	global_load_lds_dwordx4 v[234:235], off
	s_add_i32 m0, s63, 0x2000
	s_add_u32 s64, s44, 0x80000
	v_lshl_add_u64 v[236:237], s[44:45], 0, v[138:139]
	s_addc_u32 s65, s45, 0
	s_add_i32 s63, s57, s0
	global_load_lds_dwordx4 v[236:237], off
	v_lshl_add_u64 v[238:239], s[64:65], 0, v[136:137]
	s_mov_b32 m0, s63
	v_mov_b32_e32 v155, v141
	global_load_lds_dwordx4 v[238:239], off
	v_lshl_add_u64 v[238:239], s[64:65], 0, v[138:139]
	s_add_i32 m0, s63, 0x2000
	s_nop 0
	global_load_lds_dwordx4 v[238:239], off
	s_mov_b32 m0, s5
	v_lshl_add_u64 v[238:239], s[46:47], 0, v[140:141]
	global_load_lds_dwordx4 v140, s[46:47]
	s_mov_b32 m0, s6
	s_nop 0
	global_load_lds_dwordx4 v154, s[46:47]
	s_waitcnt vmcnt(8)
	s_waitcnt lgkmcnt(0)
	v_lshl_add_u64 v[154:155], s[46:47], 0, v[154:155]
	s_barrier
	s_setprio 1
	v_mfma_f32_16x16x32_bf16 v[28:31], v[170:173], v[202:205], v[28:31]
	v_mfma_f32_16x16x32_bf16 v[24:27], v[178:181], v[202:205], v[24:27]
	v_mfma_f32_16x16x32_bf16 v[20:23], v[170:173], v[210:213], v[20:23]
	v_mfma_f32_16x16x32_bf16 v[16:19], v[178:181], v[210:213], v[16:19]
	v_mfma_f32_16x16x32_bf16 v[12:15], v[170:173], v[218:221], v[12:15]
	v_mfma_f32_16x16x32_bf16 v[8:11], v[178:181], v[218:221], v[8:11]
	v_mfma_f32_16x16x32_bf16 v[4:7], v[170:173], v[226:229], v[4:7]
	v_mfma_f32_16x16x32_bf16 v[0:3], v[178:181], v[226:229], v[0:3]
	v_mfma_f32_16x16x32_bf16 v[28:31], v[174:177], v[206:209], v[28:31]
	v_mfma_f32_16x16x32_bf16 v[24:27], v[182:185], v[206:209], v[24:27]
	v_mfma_f32_16x16x32_bf16 v[20:23], v[174:177], v[214:217], v[20:23]
	v_mfma_f32_16x16x32_bf16 v[16:19], v[182:185], v[214:217], v[16:19]
	v_mfma_f32_16x16x32_bf16 v[12:15], v[174:177], v[222:225], v[12:15]
	v_mfma_f32_16x16x32_bf16 v[8:11], v[182:185], v[222:225], v[8:11]
	v_mfma_f32_16x16x32_bf16 v[4:7], v[174:177], v[230:233], v[4:7]
	v_mfma_f32_16x16x32_bf16 v[0:3], v[182:185], v[230:233], v[0:3]
	s_setprio 0
	s_setprio 1
	v_mfma_f32_16x16x32_bf16 v[92:95], v[186:189], v[202:205], v[92:95]
	v_mfma_f32_16x16x32_bf16 v[88:91], v[194:197], v[202:205], v[88:91]
	v_mfma_f32_16x16x32_bf16 v[84:87], v[186:189], v[210:213], v[84:87]
	v_mfma_f32_16x16x32_bf16 v[80:83], v[194:197], v[210:213], v[80:83]
	v_mfma_f32_16x16x32_bf16 v[72:75], v[186:189], v[218:221], v[72:75]
	v_mfma_f32_16x16x32_bf16 v[76:79], v[194:197], v[218:221], v[76:79]
	v_mfma_f32_16x16x32_bf16 v[64:67], v[186:189], v[226:229], v[64:67]
	v_mfma_f32_16x16x32_bf16 v[68:71], v[194:197], v[226:229], v[68:71]
	v_mfma_f32_16x16x32_bf16 v[92:95], v[190:193], v[206:209], v[92:95]
	v_mfma_f32_16x16x32_bf16 v[88:91], v[198:201], v[206:209], v[88:91]
	v_mfma_f32_16x16x32_bf16 v[84:87], v[190:193], v[214:217], v[84:87]
	v_mfma_f32_16x16x32_bf16 v[80:83], v[198:201], v[214:217], v[80:83]
	v_mfma_f32_16x16x32_bf16 v[72:75], v[190:193], v[222:225], v[72:75]
	v_mfma_f32_16x16x32_bf16 v[76:79], v[198:201], v[222:225], v[76:79]
	v_mfma_f32_16x16x32_bf16 v[64:67], v[190:193], v[230:233], v[64:67]
	v_mfma_f32_16x16x32_bf16 v[68:71], v[198:201], v[230:233], v[68:71]
	s_setprio 0
	s_barrier
	s_add_i32 s63, 0, 0x18000
	v_add_u32_e32 v133, s63, v161
	s_add_i32 s64, 0, 0x1c000
	ds_read_b128 v[170:173], v133
	ds_read_b128 v[174:177], v133 offset:1024
	ds_read_b128 v[178:181], v133 offset:2048
	ds_read_b128 v[182:185], v133 offset:3072
	v_add_u32_e32 v133, s64, v161
	ds_read_b128 v[186:189], v133
	ds_read_b128 v[190:193], v133 offset:1024
	ds_read_b128 v[194:197], v133 offset:2048
	ds_read_b128 v[198:201], v133 offset:3072
	s_mov_b32 m0, s7
	ds_read_b128 v[202:205], v165 offset:32768
	ds_read_b128 v[206:209], v165 offset:33792
	ds_read_b128 v[210:213], v165 offset:34816
	ds_read_b128 v[214:217], v165 offset:35840
	ds_read_b128 v[218:221], v165 offset:36864
	ds_read_b128 v[222:225], v165 offset:37888
	ds_read_b128 v[226:229], v165 offset:38912
	ds_read_b128 v[230:233], v165 offset:39936
	global_load_lds_dwordx4 v129, s[46:47]
	s_mov_b32 m0, s31
	s_nop 0
	global_load_lds_dwordx4 v131, s[46:47]
	s_waitcnt vmcnt(8)
	s_waitcnt lgkmcnt(0)
	s_barrier
	s_setprio 1
	v_mfma_f32_16x16x32_bf16 v[60:63], v[170:173], v[202:205], v[60:63]
	v_mfma_f32_16x16x32_bf16 v[56:59], v[178:181], v[202:205], v[56:59]
	v_mfma_f32_16x16x32_bf16 v[52:55], v[170:173], v[210:213], v[52:55]
	v_mfma_f32_16x16x32_bf16 v[48:51], v[178:181], v[210:213], v[48:51]
	v_mfma_f32_16x16x32_bf16 v[44:47], v[170:173], v[218:221], v[44:47]
	v_mfma_f32_16x16x32_bf16 v[40:43], v[178:181], v[218:221], v[40:43]
	v_mfma_f32_16x16x32_bf16 v[36:39], v[170:173], v[226:229], v[36:39]
	v_mfma_f32_16x16x32_bf16 v[32:35], v[178:181], v[226:229], v[32:35]
	v_mfma_f32_16x16x32_bf16 v[60:63], v[174:177], v[206:209], v[60:63]
	v_mfma_f32_16x16x32_bf16 v[56:59], v[182:185], v[206:209], v[56:59]
	v_mfma_f32_16x16x32_bf16 v[52:55], v[174:177], v[214:217], v[52:55]
	v_mfma_f32_16x16x32_bf16 v[48:51], v[182:185], v[214:217], v[48:51]
	v_mfma_f32_16x16x32_bf16 v[44:47], v[174:177], v[222:225], v[44:47]
	v_mfma_f32_16x16x32_bf16 v[40:43], v[182:185], v[222:225], v[40:43]
	v_mfma_f32_16x16x32_bf16 v[36:39], v[174:177], v[230:233], v[36:39]
	v_mfma_f32_16x16x32_bf16 v[32:35], v[182:185], v[230:233], v[32:35]
	s_setprio 0
	s_setprio 1
	v_mfma_f32_16x16x32_bf16 v[124:127], v[186:189], v[202:205], v[124:127]
	v_mfma_f32_16x16x32_bf16 v[120:123], v[194:197], v[202:205], v[120:123]
	v_mfma_f32_16x16x32_bf16 v[116:119], v[186:189], v[210:213], v[116:119]
	v_mfma_f32_16x16x32_bf16 v[112:115], v[194:197], v[210:213], v[112:115]
	v_mfma_f32_16x16x32_bf16 v[108:111], v[186:189], v[218:221], v[108:111]
	v_mfma_f32_16x16x32_bf16 v[104:107], v[194:197], v[218:221], v[104:107]
	v_mfma_f32_16x16x32_bf16 v[100:103], v[186:189], v[226:229], v[100:103]
	v_mfma_f32_16x16x32_bf16 v[96:99], v[194:197], v[226:229], v[96:99]
	v_mfma_f32_16x16x32_bf16 v[124:127], v[190:193], v[206:209], v[124:127]
	v_mfma_f32_16x16x32_bf16 v[120:123], v[198:201], v[206:209], v[120:123]
	v_mfma_f32_16x16x32_bf16 v[116:119], v[190:193], v[214:217], v[116:119]
	v_mfma_f32_16x16x32_bf16 v[112:115], v[198:201], v[214:217], v[112:115]
	v_mfma_f32_16x16x32_bf16 v[108:111], v[190:193], v[222:225], v[108:111]
	v_mfma_f32_16x16x32_bf16 v[104:107], v[198:201], v[222:225], v[104:107]
	v_mfma_f32_16x16x32_bf16 v[100:103], v[190:193], v[230:233], v[100:103]
	v_mfma_f32_16x16x32_bf16 v[96:99], v[198:201], v[230:233], v[96:99]
	s_setprio 0
	s_barrier
	s_add_i32 s46, s63, s0
	v_lshl_add_u64 v[234:235], v[234:235], 0, s[24:25]
	s_mov_b32 m0, s46
	ds_read_b128 v[202:205], v165 offset:49152
	ds_read_b128 v[206:209], v165 offset:50176
	ds_read_b128 v[210:213], v165 offset:51200
	ds_read_b128 v[214:217], v165 offset:52224
	ds_read_b128 v[218:221], v165 offset:53248
	ds_read_b128 v[222:225], v165 offset:54272
	ds_read_b128 v[226:229], v165 offset:55296
	ds_read_b128 v[230:233], v165 offset:56320
	global_load_lds_dwordx4 v[234:235], off
	s_add_i32 m0, s46, 0x2000
	s_add_u32 s44, s44, 0x80080
	v_lshl_add_u64 v[234:235], v[236:237], 0, s[24:25]
	s_addc_u32 s45, s45, 0
	s_add_i32 s46, s64, s0
	global_load_lds_dwordx4 v[234:235], off
	v_lshl_add_u64 v[234:235], s[44:45], 0, v[136:137]
	s_mov_b32 m0, s46
	v_lshl_add_u64 v[154:155], v[154:155], 0, s[24:25]
	global_load_lds_dwordx4 v[234:235], off
	v_lshl_add_u64 v[234:235], s[44:45], 0, v[138:139]
	s_add_i32 m0, s46, 0x2000
	s_nop 0
	global_load_lds_dwordx4 v[234:235], off
	v_lshl_add_u64 v[234:235], v[238:239], 0, s[24:25]
	s_mov_b32 m0, s49
	s_nop 0
	global_load_lds_dwordx4 v[234:235], off
	s_mov_b32 m0, s51
	s_nop 0
	global_load_lds_dwordx4 v[154:155], off
	s_waitcnt vmcnt(8)
	s_waitcnt lgkmcnt(0)
	s_barrier
	s_setprio 1
	v_mfma_f32_16x16x32_bf16 v[28:31], v[170:173], v[202:205], v[28:31]
	v_mfma_f32_16x16x32_bf16 v[24:27], v[178:181], v[202:205], v[24:27]
	v_mfma_f32_16x16x32_bf16 v[20:23], v[170:173], v[210:213], v[20:23]
	v_mfma_f32_16x16x32_bf16 v[16:19], v[178:181], v[210:213], v[16:19]
	v_mfma_f32_16x16x32_bf16 v[12:15], v[170:173], v[218:221], v[12:15]
	v_mfma_f32_16x16x32_bf16 v[8:11], v[178:181], v[218:221], v[8:11]
	v_mfma_f32_16x16x32_bf16 v[4:7], v[170:173], v[226:229], v[4:7]
	v_mfma_f32_16x16x32_bf16 v[0:3], v[178:181], v[226:229], v[0:3]
	v_mfma_f32_16x16x32_bf16 v[28:31], v[174:177], v[206:209], v[28:31]
	v_mfma_f32_16x16x32_bf16 v[24:27], v[182:185], v[206:209], v[24:27]
	v_mfma_f32_16x16x32_bf16 v[20:23], v[174:177], v[214:217], v[20:23]
	v_mfma_f32_16x16x32_bf16 v[16:19], v[182:185], v[214:217], v[16:19]
	v_mfma_f32_16x16x32_bf16 v[12:15], v[174:177], v[222:225], v[12:15]
	v_mfma_f32_16x16x32_bf16 v[8:11], v[182:185], v[222:225], v[8:11]
	v_mfma_f32_16x16x32_bf16 v[4:7], v[174:177], v[230:233], v[4:7]
	v_mfma_f32_16x16x32_bf16 v[0:3], v[182:185], v[230:233], v[0:3]
	s_setprio 0
	s_setprio 1
	v_mfma_f32_16x16x32_bf16 v[92:95], v[186:189], v[202:205], v[92:95]
	v_mfma_f32_16x16x32_bf16 v[88:91], v[194:197], v[202:205], v[88:91]
	v_mfma_f32_16x16x32_bf16 v[84:87], v[186:189], v[210:213], v[84:87]
	v_mfma_f32_16x16x32_bf16 v[80:83], v[194:197], v[210:213], v[80:83]
	v_mfma_f32_16x16x32_bf16 v[72:75], v[186:189], v[218:221], v[72:75]
	v_mfma_f32_16x16x32_bf16 v[76:79], v[194:197], v[218:221], v[76:79]
	v_mfma_f32_16x16x32_bf16 v[64:67], v[186:189], v[226:229], v[64:67]
	v_mfma_f32_16x16x32_bf16 v[68:71], v[194:197], v[226:229], v[68:71]
	v_mfma_f32_16x16x32_bf16 v[92:95], v[190:193], v[206:209], v[92:95]
	v_mfma_f32_16x16x32_bf16 v[88:91], v[198:201], v[206:209], v[88:91]
	v_mfma_f32_16x16x32_bf16 v[84:87], v[190:193], v[214:217], v[84:87]
	v_mfma_f32_16x16x32_bf16 v[80:83], v[198:201], v[214:217], v[80:83]
	v_mfma_f32_16x16x32_bf16 v[72:75], v[190:193], v[222:225], v[72:75]
	v_mfma_f32_16x16x32_bf16 v[76:79], v[198:201], v[222:225], v[76:79]
	v_mfma_f32_16x16x32_bf16 v[64:67], v[190:193], v[230:233], v[64:67]
	v_mfma_f32_16x16x32_bf16 v[68:71], v[198:201], v[230:233], v[68:71]
	s_setprio 0
	s_add_i32 s62, s62, 2
	s_add_u32 s10, s10, 0x100
	s_addc_u32 s11, s11, 0
	s_cmp_gt_u32 s62, 29
	s_barrier
	s_cbranch_scc0 .LBB0_1571
	s_and_b64 vcc, exec, s[26:27]
	s_cbranch_vccnz .LBB0_1575
	v_lshl_add_u32 v150, s61, 8, v160
	s_cmp_lg_u32 s12, 46
	s_mov_b64 s[10:11], -1
	s_cbranch_scc1 .LBB0_1576

.LBB0_2279:
	s_add_i32 s65, s30, 2
	s_add_u32 s31, s24, s28
	s_addc_u32 s34, s25, s29
	v_add_u32_e32 v131, s46, v152
	s_add_u32 s66, s31, 0x100
	ds_read_b128 v[160:163], v131
	ds_read_b128 v[164:167], v131 offset:1024
	ds_read_b128 v[168:171], v131 offset:2048
	ds_read_b128 v[172:175], v131 offset:3072
	v_add_u32_e32 v131, s47, v152
	s_addc_u32 s34, s34, 0
	ds_read_b128 v[176:179], v131
	ds_read_b128 v[180:183], v131 offset:1024
	ds_read_b128 v[184:187], v131 offset:2048
	ds_read_b128 v[188:191], v131 offset:3072
	s_add_u32 s67, s63, s28
	s_addc_u32 s68, s64, s29
	s_cmp_eq_u32 s62, s30
	s_cselect_b64 vcc, -1, 0
	s_and_b64 s[30:31], vcc, exec
	s_cselect_b32 s30, s59, s67
	v_cndmask_b32_e32 v136, v128, v156, vcc
	s_cselect_b32 s35, s60, s34
	s_cselect_b32 s34, s61, s66
	v_cndmask_b32_e32 v129, v138, v158, vcc
	v_cndmask_b32_e32 v224, v130, v157, vcc
	v_cndmask_b32_e32 v131, v140, v159, vcc
	s_cselect_b32 s31, s19, s68
	v_lshl_add_u64 v[226:227], v[146:147], 0, s[28:29]
	s_add_i32 m0, s36, 0xc000
	ds_read_b128 v[192:195], v155
	ds_read_b128 v[196:199], v155 offset:1024
	ds_read_b128 v[200:203], v155 offset:2048
	ds_read_b128 v[204:207], v155 offset:3072
	ds_read_b128 v[208:211], v155 offset:4096
	ds_read_b128 v[212:215], v155 offset:5120
	ds_read_b128 v[216:219], v155 offset:6144
	ds_read_b128 v[220:223], v155 offset:7168
	global_load_lds_dwordx4 v[226:227], off
	v_lshl_add_u64 v[226:227], v[142:143], 0, s[28:29]
	s_add_i32 m0, s36, 0xe000
	s_nop 0
	global_load_lds_dwordx4 v[226:227], off
	s_waitcnt vmcnt(8)
	s_waitcnt lgkmcnt(0)
	s_barrier
	s_setprio 1
	v_mfma_f32_16x16x32_bf16 v[108:111], v[160:163], v[192:195], v[108:111]
	v_mfma_f32_16x16x32_bf16 v[104:107], v[168:171], v[192:195], v[104:107]
	v_mfma_f32_16x16x32_bf16 v[100:103], v[160:163], v[200:203], v[100:103]
	v_mfma_f32_16x16x32_bf16 v[96:99], v[168:171], v[200:203], v[96:99]
	v_mfma_f32_16x16x32_bf16 v[92:95], v[160:163], v[208:211], v[92:95]
	v_mfma_f32_16x16x32_bf16 v[88:91], v[168:171], v[208:211], v[88:91]
	v_mfma_f32_16x16x32_bf16 v[84:87], v[160:163], v[216:219], v[84:87]
	v_mfma_f32_16x16x32_bf16 v[80:83], v[168:171], v[216:219], v[80:83]
	v_mfma_f32_16x16x32_bf16 v[108:111], v[164:167], v[196:199], v[108:111]
	v_mfma_f32_16x16x32_bf16 v[104:107], v[172:175], v[196:199], v[104:107]
	v_mfma_f32_16x16x32_bf16 v[100:103], v[164:167], v[204:207], v[100:103]
	v_mfma_f32_16x16x32_bf16 v[96:99], v[172:175], v[204:207], v[96:99]
	v_mfma_f32_16x16x32_bf16 v[92:95], v[164:167], v[212:215], v[92:95]
	v_mfma_f32_16x16x32_bf16 v[88:91], v[172:175], v[212:215], v[88:91]
	v_mfma_f32_16x16x32_bf16 v[84:87], v[164:167], v[220:223], v[84:87]
	v_mfma_f32_16x16x32_bf16 v[80:83], v[172:175], v[220:223], v[80:83]
	s_setprio 0
	s_setprio 1
	v_mfma_f32_16x16x32_bf16 v[76:79], v[176:179], v[192:195], v[76:79]
	v_mfma_f32_16x16x32_bf16 v[72:75], v[184:187], v[192:195], v[72:75]
	v_mfma_f32_16x16x32_bf16 v[68:71], v[176:179], v[200:203], v[68:71]
	v_mfma_f32_16x16x32_bf16 v[64:67], v[184:187], v[200:203], v[64:67]
	v_mfma_f32_16x16x32_bf16 v[60:63], v[176:179], v[208:211], v[60:63]
	v_mfma_f32_16x16x32_bf16 v[56:59], v[184:187], v[208:211], v[56:59]
	v_mfma_f32_16x16x32_bf16 v[52:55], v[176:179], v[216:219], v[52:55]
	v_mfma_f32_16x16x32_bf16 v[48:51], v[184:187], v[216:219], v[48:51]
	v_mfma_f32_16x16x32_bf16 v[76:79], v[180:183], v[196:199], v[76:79]
	v_mfma_f32_16x16x32_bf16 v[72:75], v[188:191], v[196:199], v[72:75]
	v_mfma_f32_16x16x32_bf16 v[68:71], v[180:183], v[204:207], v[68:71]
	v_mfma_f32_16x16x32_bf16 v[64:67], v[188:191], v[204:207], v[64:67]
	v_mfma_f32_16x16x32_bf16 v[60:63], v[180:183], v[212:215], v[60:63]
	v_mfma_f32_16x16x32_bf16 v[56:59], v[188:191], v[212:215], v[56:59]
	v_mfma_f32_16x16x32_bf16 v[52:55], v[180:183], v[220:223], v[52:55]
	v_mfma_f32_16x16x32_bf16 v[48:51], v[188:191], v[220:223], v[48:51]
	s_setprio 0
	s_barrier
	s_add_i32 s66, s46, s5
	v_lshl_add_u64 v[226:227], s[30:31], 0, v[132:133]
	s_mov_b32 m0, s66
	ds_read_b128 v[192:195], v155 offset:16384
	ds_read_b128 v[196:199], v155 offset:17408
	ds_read_b128 v[200:203], v155 offset:18432
	ds_read_b128 v[204:207], v155 offset:19456
	ds_read_b128 v[208:211], v155 offset:20480
	ds_read_b128 v[212:215], v155 offset:21504
	ds_read_b128 v[216:219], v155 offset:22528
	ds_read_b128 v[220:223], v155 offset:23552
	global_load_lds_dwordx4 v[226:227], off
	s_add_i32 m0, s66, 0x2000
	s_add_u32 s66, s30, 0x80000
	v_lshl_add_u64 v[228:229], s[30:31], 0, v[134:135]
	s_addc_u32 s67, s31, 0
	s_add_i32 s68, s47, s5
	global_load_lds_dwordx4 v[228:229], off
	v_lshl_add_u64 v[230:231], s[66:67], 0, v[132:133]
	s_mov_b32 m0, s68
	v_mov_b32_e32 v225, v137
	global_load_lds_dwordx4 v[230:231], off
	v_lshl_add_u64 v[230:231], s[66:67], 0, v[134:135]
	s_add_i32 m0, s68, 0x2000
	s_nop 0
	global_load_lds_dwordx4 v[230:231], off
	s_mov_b32 m0, s36
	v_lshl_add_u64 v[230:231], s[34:35], 0, v[136:137]
	global_load_lds_dwordx4 v136, s[34:35]
	s_mov_b32 m0, s37
	s_nop 0
	global_load_lds_dwordx4 v224, s[34:35]
	s_waitcnt vmcnt(8)
	s_waitcnt lgkmcnt(0)
	v_lshl_add_u64 v[224:225], s[34:35], 0, v[224:225]
	s_barrier
	s_setprio 1
	v_mfma_f32_16x16x32_bf16 v[44:47], v[160:163], v[192:195], v[44:47]
	v_mfma_f32_16x16x32_bf16 v[40:43], v[168:171], v[192:195], v[40:43]
	v_mfma_f32_16x16x32_bf16 v[36:39], v[160:163], v[200:203], v[36:39]
	v_mfma_f32_16x16x32_bf16 v[32:35], v[168:171], v[200:203], v[32:35]
	v_mfma_f32_16x16x32_bf16 v[28:31], v[160:163], v[208:211], v[28:31]
	v_mfma_f32_16x16x32_bf16 v[24:27], v[168:171], v[208:211], v[24:27]
	v_mfma_f32_16x16x32_bf16 v[20:23], v[160:163], v[216:219], v[20:23]
	v_mfma_f32_16x16x32_bf16 v[16:19], v[168:171], v[216:219], v[16:19]
	v_mfma_f32_16x16x32_bf16 v[44:47], v[164:167], v[196:199], v[44:47]
	v_mfma_f32_16x16x32_bf16 v[40:43], v[172:175], v[196:199], v[40:43]
	v_mfma_f32_16x16x32_bf16 v[36:39], v[164:167], v[204:207], v[36:39]
	v_mfma_f32_16x16x32_bf16 v[32:35], v[172:175], v[204:207], v[32:35]
	v_mfma_f32_16x16x32_bf16 v[28:31], v[164:167], v[212:215], v[28:31]
	v_mfma_f32_16x16x32_bf16 v[24:27], v[172:175], v[212:215], v[24:27]
	v_mfma_f32_16x16x32_bf16 v[20:23], v[164:167], v[220:223], v[20:23]
	v_mfma_f32_16x16x32_bf16 v[16:19], v[172:175], v[220:223], v[16:19]
	s_setprio 0
	s_setprio 1
	v_mfma_f32_16x16x32_bf16 v[12:15], v[176:179], v[192:195], v[12:15]
	v_mfma_f32_16x16x32_bf16 v[8:11], v[184:187], v[192:195], v[8:11]
	v_mfma_f32_16x16x32_bf16 v[4:7], v[176:179], v[200:203], v[4:7]
	v_mfma_f32_16x16x32_bf16 v[0:3], v[184:187], v[200:203], v[0:3]
	v_mfma_f32_16x16x32_bf16 v[112:115], v[176:179], v[208:211], v[112:115]
	v_mfma_f32_16x16x32_bf16 v[116:119], v[184:187], v[208:211], v[116:119]
	v_mfma_f32_16x16x32_bf16 v[120:123], v[176:179], v[216:219], v[120:123]
	v_mfma_f32_16x16x32_bf16 v[124:127], v[184:187], v[216:219], v[124:127]
	v_mfma_f32_16x16x32_bf16 v[12:15], v[180:183], v[196:199], v[12:15]
	v_mfma_f32_16x16x32_bf16 v[8:11], v[188:191], v[196:199], v[8:11]
	v_mfma_f32_16x16x32_bf16 v[4:7], v[180:183], v[204:207], v[4:7]
	v_mfma_f32_16x16x32_bf16 v[0:3], v[188:191], v[204:207], v[0:3]
	v_mfma_f32_16x16x32_bf16 v[112:115], v[180:183], v[212:215], v[112:115]
	v_mfma_f32_16x16x32_bf16 v[116:119], v[188:191], v[212:215], v[116:119]
	v_mfma_f32_16x16x32_bf16 v[120:123], v[180:183], v[220:223], v[120:123]
	v_mfma_f32_16x16x32_bf16 v[124:127], v[188:191], v[220:223], v[124:127]
	s_setprio 0
	s_barrier
	s_add_i32 s66, 0, 0x18000
	v_add_u32_e32 v136, s66, v152
	s_add_i32 s67, 0, 0x1c000
	ds_read_b128 v[160:163], v136
	ds_read_b128 v[164:167], v136 offset:1024
	ds_read_b128 v[168:171], v136 offset:2048
	ds_read_b128 v[172:175], v136 offset:3072
	v_add_u32_e32 v136, s67, v152
	ds_read_b128 v[176:179], v136
	ds_read_b128 v[180:183], v136 offset:1024
	ds_read_b128 v[184:187], v136 offset:2048
	ds_read_b128 v[188:191], v136 offset:3072
	s_mov_b32 m0, s38
	ds_read_b128 v[192:195], v155 offset:32768
	ds_read_b128 v[196:199], v155 offset:33792
	ds_read_b128 v[200:203], v155 offset:34816
	ds_read_b128 v[204:207], v155 offset:35840
	ds_read_b128 v[208:211], v155 offset:36864
	ds_read_b128 v[212:215], v155 offset:37888
	ds_read_b128 v[216:219], v155 offset:38912
	ds_read_b128 v[220:223], v155 offset:39936
	global_load_lds_dwordx4 v129, s[34:35]
	s_mov_b32 m0, s39
	s_nop 0
	global_load_lds_dwordx4 v131, s[34:35]
	s_waitcnt vmcnt(8)
	s_waitcnt lgkmcnt(0)
	s_barrier
	s_setprio 1
	v_mfma_f32_16x16x32_bf16 v[108:111], v[160:163], v[192:195], v[108:111]
	v_mfma_f32_16x16x32_bf16 v[104:107], v[168:171], v[192:195], v[104:107]
	v_mfma_f32_16x16x32_bf16 v[100:103], v[160:163], v[200:203], v[100:103]
	v_mfma_f32_16x16x32_bf16 v[96:99], v[168:171], v[200:203], v[96:99]
	v_mfma_f32_16x16x32_bf16 v[92:95], v[160:163], v[208:211], v[92:95]
	v_mfma_f32_16x16x32_bf16 v[88:91], v[168:171], v[208:211], v[88:91]
	v_mfma_f32_16x16x32_bf16 v[84:87], v[160:163], v[216:219], v[84:87]
	v_mfma_f32_16x16x32_bf16 v[80:83], v[168:171], v[216:219], v[80:83]
	v_mfma_f32_16x16x32_bf16 v[108:111], v[164:167], v[196:199], v[108:111]
	v_mfma_f32_16x16x32_bf16 v[104:107], v[172:175], v[196:199], v[104:107]
	v_mfma_f32_16x16x32_bf16 v[100:103], v[164:167], v[204:207], v[100:103]
	v_mfma_f32_16x16x32_bf16 v[96:99], v[172:175], v[204:207], v[96:99]
	v_mfma_f32_16x16x32_bf16 v[92:95], v[164:167], v[212:215], v[92:95]
	v_mfma_f32_16x16x32_bf16 v[88:91], v[172:175], v[212:215], v[88:91]
	v_mfma_f32_16x16x32_bf16 v[84:87], v[164:167], v[220:223], v[84:87]
	v_mfma_f32_16x16x32_bf16 v[80:83], v[172:175], v[220:223], v[80:83]
	s_setprio 0
	s_setprio 1
	v_mfma_f32_16x16x32_bf16 v[76:79], v[176:179], v[192:195], v[76:79]
	v_mfma_f32_16x16x32_bf16 v[72:75], v[184:187], v[192:195], v[72:75]
	v_mfma_f32_16x16x32_bf16 v[68:71], v[176:179], v[200:203], v[68:71]
	v_mfma_f32_16x16x32_bf16 v[64:67], v[184:187], v[200:203], v[64:67]
	v_mfma_f32_16x16x32_bf16 v[60:63], v[176:179], v[208:211], v[60:63]
	v_mfma_f32_16x16x32_bf16 v[56:59], v[184:187], v[208:211], v[56:59]
	v_mfma_f32_16x16x32_bf16 v[52:55], v[176:179], v[216:219], v[52:55]
	v_mfma_f32_16x16x32_bf16 v[48:51], v[184:187], v[216:219], v[48:51]
	v_mfma_f32_16x16x32_bf16 v[76:79], v[180:183], v[196:199], v[76:79]
	v_mfma_f32_16x16x32_bf16 v[72:75], v[188:191], v[196:199], v[72:75]
	v_mfma_f32_16x16x32_bf16 v[68:71], v[180:183], v[204:207], v[68:71]
	v_mfma_f32_16x16x32_bf16 v[64:67], v[188:191], v[204:207], v[64:67]
	v_mfma_f32_16x16x32_bf16 v[60:63], v[180:183], v[212:215], v[60:63]
	v_mfma_f32_16x16x32_bf16 v[56:59], v[188:191], v[212:215], v[56:59]
	v_mfma_f32_16x16x32_bf16 v[52:55], v[180:183], v[220:223], v[52:55]
	v_mfma_f32_16x16x32_bf16 v[48:51], v[188:191], v[220:223], v[48:51]
	s_setprio 0
	s_barrier
	s_add_i32 s34, s66, s5
	v_lshl_add_u64 v[226:227], v[226:227], 0, s[12:13]
	s_mov_b32 m0, s34
	ds_read_b128 v[192:195], v155 offset:49152
	ds_read_b128 v[196:199], v155 offset:50176
	ds_read_b128 v[200:203], v155 offset:51200
	ds_read_b128 v[204:207], v155 offset:52224
	ds_read_b128 v[208:211], v155 offset:53248
	ds_read_b128 v[212:215], v155 offset:54272
	ds_read_b128 v[216:219], v155 offset:55296
	ds_read_b128 v[220:223], v155 offset:56320
	global_load_lds_dwordx4 v[226:227], off
	s_add_i32 m0, s34, 0x2000
	s_add_u32 s30, s30, 0x80080
	v_lshl_add_u64 v[226:227], v[228:229], 0, s[12:13]
	s_addc_u32 s31, s31, 0
	s_add_i32 s34, s67, s5
	global_load_lds_dwordx4 v[226:227], off
	v_lshl_add_u64 v[226:227], s[30:31], 0, v[132:133]
	s_mov_b32 m0, s34
	v_lshl_add_u64 v[224:225], v[224:225], 0, s[12:13]
	global_load_lds_dwordx4 v[226:227], off
	v_lshl_add_u64 v[226:227], s[30:31], 0, v[134:135]
	s_add_i32 m0, s34, 0x2000
	s_nop 0
	global_load_lds_dwordx4 v[226:227], off
	v_lshl_add_u64 v[226:227], v[230:231], 0, s[12:13]
	s_mov_b32 m0, s42
	s_nop 0
	global_load_lds_dwordx4 v[226:227], off
	s_mov_b32 m0, s43
	s_nop 0
	global_load_lds_dwordx4 v[224:225], off
	s_waitcnt vmcnt(8)
	s_waitcnt lgkmcnt(0)
	s_barrier
	s_setprio 1
	v_mfma_f32_16x16x32_bf16 v[44:47], v[160:163], v[192:195], v[44:47]
	v_mfma_f32_16x16x32_bf16 v[40:43], v[168:171], v[192:195], v[40:43]
	v_mfma_f32_16x16x32_bf16 v[36:39], v[160:163], v[200:203], v[36:39]
	v_mfma_f32_16x16x32_bf16 v[32:35], v[168:171], v[200:203], v[32:35]
	v_mfma_f32_16x16x32_bf16 v[28:31], v[160:163], v[208:211], v[28:31]
	v_mfma_f32_16x16x32_bf16 v[24:27], v[168:171], v[208:211], v[24:27]
	v_mfma_f32_16x16x32_bf16 v[20:23], v[160:163], v[216:219], v[20:23]
	v_mfma_f32_16x16x32_bf16 v[16:19], v[168:171], v[216:219], v[16:19]
	v_mfma_f32_16x16x32_bf16 v[44:47], v[164:167], v[196:199], v[44:47]
	v_mfma_f32_16x16x32_bf16 v[40:43], v[172:175], v[196:199], v[40:43]
	v_mfma_f32_16x16x32_bf16 v[36:39], v[164:167], v[204:207], v[36:39]
	v_mfma_f32_16x16x32_bf16 v[32:35], v[172:175], v[204:207], v[32:35]
	v_mfma_f32_16x16x32_bf16 v[28:31], v[164:167], v[212:215], v[28:31]
	v_mfma_f32_16x16x32_bf16 v[24:27], v[172:175], v[212:215], v[24:27]
	v_mfma_f32_16x16x32_bf16 v[20:23], v[164:167], v[220:223], v[20:23]
	v_mfma_f32_16x16x32_bf16 v[16:19], v[172:175], v[220:223], v[16:19]
	s_setprio 0
	s_setprio 1
	v_mfma_f32_16x16x32_bf16 v[12:15], v[176:179], v[192:195], v[12:15]
	v_mfma_f32_16x16x32_bf16 v[8:11], v[184:187], v[192:195], v[8:11]
	v_mfma_f32_16x16x32_bf16 v[4:7], v[176:179], v[200:203], v[4:7]
	v_mfma_f32_16x16x32_bf16 v[0:3], v[184:187], v[200:203], v[0:3]
	v_mfma_f32_16x16x32_bf16 v[112:115], v[176:179], v[208:211], v[112:115]
	v_mfma_f32_16x16x32_bf16 v[116:119], v[184:187], v[208:211], v[116:119]
	v_mfma_f32_16x16x32_bf16 v[120:123], v[176:179], v[216:219], v[120:123]
	v_mfma_f32_16x16x32_bf16 v[124:127], v[184:187], v[216:219], v[124:127]
	v_mfma_f32_16x16x32_bf16 v[12:15], v[180:183], v[196:199], v[12:15]
	v_mfma_f32_16x16x32_bf16 v[8:11], v[188:191], v[196:199], v[8:11]
	v_mfma_f32_16x16x32_bf16 v[4:7], v[180:183], v[204:207], v[4:7]
	v_mfma_f32_16x16x32_bf16 v[0:3], v[188:191], v[204:207], v[0:3]
	v_mfma_f32_16x16x32_bf16 v[112:115], v[180:183], v[212:215], v[112:115]
	v_mfma_f32_16x16x32_bf16 v[116:119], v[188:191], v[212:215], v[116:119]
	v_mfma_f32_16x16x32_bf16 v[120:123], v[180:183], v[220:223], v[120:123]
	v_mfma_f32_16x16x32_bf16 v[124:127], v[188:191], v[220:223], v[124:127]
	s_setprio 0
	s_add_u32 s28, s28, 0x100
	s_addc_u32 s29, s29, 0
	s_cmp_ge_i32 s65, s57
	s_mov_b32 s30, s65
	s_barrier
	s_cbranch_scc0 .LBB0_2279
	s_and_b64 vcc, exec, s[14:15]
	s_cbranch_vccz .LBB0_2282
	s_barrier

.LBB0_2355:
	ds_read_b128 v[140:143], v162
	ds_read_b128 v[170:173], v162 offset:1024
	ds_read_b128 v[174:177], v162 offset:2048
	ds_read_b128 v[178:181], v162 offset:3072
	ds_read_b128 v[182:185], v163
	ds_read_b128 v[186:189], v163 offset:1024
	ds_read_b128 v[190:193], v163 offset:2048
	ds_read_b128 v[194:197], v163 offset:3072
	s_add_u32 s42, s38, s8
	s_addc_u32 s43, s39, s9
	s_cmpk_eq_i32 s8, 0x1000
	s_cselect_b64 vcc, -1, 0
	s_and_b64 s[40:41], vcc, exec
	s_cselect_b32 s68, 0, s8
	s_cselect_b32 s67, 0, s9
	s_cselect_b32 s40, s65, s42
	s_cselect_b32 s41, s35, s43
	s_add_u32 s42, s10, s68
	v_cndmask_b32_e32 v150, v128, v165, vcc
	v_cndmask_b32_e32 v129, v132, v167, vcc
	v_cndmask_b32_e32 v230, v130, v166, vcc
	v_cndmask_b32_e32 v131, v134, v168, vcc
	s_addc_u32 s43, s11, s67
	v_lshl_add_u64 v[232:233], v[138:139], 0, s[8:9]
	v_lshl_add_u64 v[232:233], v[232:233], 0, s[24:25]
	s_add_i32 m0, s44, 0xc000
	ds_read_b128 v[198:201], v164
	ds_read_b128 v[202:205], v164 offset:1024
	ds_read_b128 v[206:209], v164 offset:2048
	ds_read_b128 v[210:213], v164 offset:3072
	ds_read_b128 v[214:217], v164 offset:4096
	ds_read_b128 v[218:221], v164 offset:5120
	ds_read_b128 v[222:225], v164 offset:6144
	ds_read_b128 v[226:229], v164 offset:7168
	global_load_lds_dwordx4 v[232:233], off
	v_lshl_add_u64 v[232:233], v[136:137], 0, s[8:9]
	v_lshl_add_u64 v[232:233], v[232:233], 0, s[24:25]
	s_add_i32 m0, s44, 0xe000
	s_nop 0
	global_load_lds_dwordx4 v[232:233], off
	s_waitcnt vmcnt(8)
	s_waitcnt lgkmcnt(0)
	s_barrier
	s_setprio 1
	v_mfma_f32_16x16x32_bf16 v[124:127], v[140:143], v[198:201], v[124:127]
	v_mfma_f32_16x16x32_bf16 v[120:123], v[174:177], v[198:201], v[120:123]
	v_mfma_f32_16x16x32_bf16 v[116:119], v[140:143], v[206:209], v[116:119]
	v_mfma_f32_16x16x32_bf16 v[112:115], v[174:177], v[206:209], v[112:115]
	v_mfma_f32_16x16x32_bf16 v[108:111], v[140:143], v[214:217], v[108:111]
	v_mfma_f32_16x16x32_bf16 v[100:103], v[174:177], v[214:217], v[100:103]
	v_mfma_f32_16x16x32_bf16 v[92:95], v[140:143], v[222:225], v[92:95]
	v_mfma_f32_16x16x32_bf16 v[84:87], v[174:177], v[222:225], v[84:87]
	v_mfma_f32_16x16x32_bf16 v[124:127], v[170:173], v[202:205], v[124:127]
	v_mfma_f32_16x16x32_bf16 v[120:123], v[178:181], v[202:205], v[120:123]
	v_mfma_f32_16x16x32_bf16 v[116:119], v[170:173], v[210:213], v[116:119]
	v_mfma_f32_16x16x32_bf16 v[112:115], v[178:181], v[210:213], v[112:115]
	v_mfma_f32_16x16x32_bf16 v[108:111], v[170:173], v[218:221], v[108:111]
	v_mfma_f32_16x16x32_bf16 v[100:103], v[178:181], v[218:221], v[100:103]
	v_mfma_f32_16x16x32_bf16 v[92:95], v[170:173], v[226:229], v[92:95]
	v_mfma_f32_16x16x32_bf16 v[84:87], v[178:181], v[226:229], v[84:87]
	s_setprio 0
	s_setprio 1
	v_mfma_f32_16x16x32_bf16 v[104:107], v[182:185], v[198:201], v[104:107]
	v_mfma_f32_16x16x32_bf16 v[96:99], v[190:193], v[198:201], v[96:99]
	v_mfma_f32_16x16x32_bf16 v[88:91], v[182:185], v[206:209], v[88:91]
	v_mfma_f32_16x16x32_bf16 v[80:83], v[190:193], v[206:209], v[80:83]
	v_mfma_f32_16x16x32_bf16 v[76:79], v[182:185], v[214:217], v[76:79]
	v_mfma_f32_16x16x32_bf16 v[72:75], v[190:193], v[214:217], v[72:75]
	v_mfma_f32_16x16x32_bf16 v[68:71], v[182:185], v[222:225], v[68:71]
	v_mfma_f32_16x16x32_bf16 v[64:67], v[190:193], v[222:225], v[64:67]
	v_mfma_f32_16x16x32_bf16 v[104:107], v[186:189], v[202:205], v[104:107]
	v_mfma_f32_16x16x32_bf16 v[96:99], v[194:197], v[202:205], v[96:99]
	v_mfma_f32_16x16x32_bf16 v[88:91], v[186:189], v[210:213], v[88:91]
	v_mfma_f32_16x16x32_bf16 v[80:83], v[194:197], v[210:213], v[80:83]
	v_mfma_f32_16x16x32_bf16 v[76:79], v[186:189], v[218:221], v[76:79]
	v_mfma_f32_16x16x32_bf16 v[72:75], v[194:197], v[218:221], v[72:75]
	v_mfma_f32_16x16x32_bf16 v[68:71], v[186:189], v[226:229], v[68:71]
	v_mfma_f32_16x16x32_bf16 v[64:67], v[194:197], v[226:229], v[64:67]
	s_setprio 0
	s_barrier
	s_add_i32 s67, s53, s5
	v_lshl_add_u64 v[232:233], s[40:41], 0, v[146:147]
	s_mov_b32 m0, s67
	ds_read_b128 v[198:201], v164 offset:16384
	ds_read_b128 v[202:205], v164 offset:17408
	ds_read_b128 v[206:209], v164 offset:18432
	ds_read_b128 v[210:213], v164 offset:19456
	ds_read_b128 v[214:217], v164 offset:20480
	ds_read_b128 v[218:221], v164 offset:21504
	ds_read_b128 v[222:225], v164 offset:22528
	ds_read_b128 v[226:229], v164 offset:23552
	global_load_lds_dwordx4 v[232:233], off
	s_add_i32 m0, s67, 0x2000
	s_add_u32 s68, s40, 0x80000
	v_lshl_add_u64 v[234:235], s[40:41], 0, v[148:149]
	s_addc_u32 s69, s41, 0
	s_add_i32 s67, s55, s5
	global_load_lds_dwordx4 v[234:235], off
	v_lshl_add_u64 v[236:237], s[68:69], 0, v[146:147]
	s_mov_b32 m0, s67
	v_mov_b32_e32 v231, v151
	global_load_lds_dwordx4 v[236:237], off
	v_lshl_add_u64 v[236:237], s[68:69], 0, v[148:149]
	s_add_i32 m0, s67, 0x2000
	s_nop 0
	global_load_lds_dwordx4 v[236:237], off
	s_mov_b32 m0, s44
	v_lshl_add_u64 v[236:237], s[42:43], 0, v[150:151]
	global_load_lds_dwordx4 v150, s[42:43]
	s_mov_b32 m0, s45
	s_nop 0
	global_load_lds_dwordx4 v230, s[42:43]
	s_waitcnt vmcnt(8)
	s_waitcnt lgkmcnt(0)
	v_lshl_add_u64 v[230:231], s[42:43], 0, v[230:231]
	s_barrier
	s_setprio 1
	v_mfma_f32_16x16x32_bf16 v[60:63], v[140:143], v[198:201], v[60:63]
	v_mfma_f32_16x16x32_bf16 v[56:59], v[174:177], v[198:201], v[56:59]
	v_mfma_f32_16x16x32_bf16 v[44:47], v[140:143], v[206:209], v[44:47]
	v_mfma_f32_16x16x32_bf16 v[36:39], v[174:177], v[206:209], v[36:39]
	v_mfma_f32_16x16x32_bf16 v[20:23], v[140:143], v[214:217], v[20:23]
	v_mfma_f32_16x16x32_bf16 v[12:15], v[174:177], v[214:217], v[12:15]
	v_mfma_f32_16x16x32_bf16 v[4:7], v[140:143], v[222:225], v[4:7]
	v_mfma_f32_16x16x32_bf16 v[0:3], v[174:177], v[222:225], v[0:3]
	v_mfma_f32_16x16x32_bf16 v[60:63], v[170:173], v[202:205], v[60:63]
	v_mfma_f32_16x16x32_bf16 v[56:59], v[178:181], v[202:205], v[56:59]
	v_mfma_f32_16x16x32_bf16 v[44:47], v[170:173], v[210:213], v[44:47]
	v_mfma_f32_16x16x32_bf16 v[36:39], v[178:181], v[210:213], v[36:39]
	v_mfma_f32_16x16x32_bf16 v[20:23], v[170:173], v[218:221], v[20:23]
	v_mfma_f32_16x16x32_bf16 v[12:15], v[178:181], v[218:221], v[12:15]
	v_mfma_f32_16x16x32_bf16 v[4:7], v[170:173], v[226:229], v[4:7]
	v_mfma_f32_16x16x32_bf16 v[0:3], v[178:181], v[226:229], v[0:3]
	s_setprio 0
	s_setprio 1
	v_mfma_f32_16x16x32_bf16 v[40:43], v[182:185], v[198:201], v[40:43]
	v_mfma_f32_16x16x32_bf16 v[32:35], v[190:193], v[198:201], v[32:35]
	v_mfma_f32_16x16x32_bf16 v[16:19], v[182:185], v[206:209], v[16:19]
	v_mfma_f32_16x16x32_bf16 v[8:11], v[190:193], v[206:209], v[8:11]
	v_mfma_f32_16x16x32_bf16 v[48:51], v[182:185], v[214:217], v[48:51]
	v_mfma_f32_16x16x32_bf16 v[52:55], v[190:193], v[214:217], v[52:55]
	v_mfma_f32_16x16x32_bf16 v[24:27], v[182:185], v[222:225], v[24:27]
	v_mfma_f32_16x16x32_bf16 v[28:31], v[190:193], v[222:225], v[28:31]
	v_mfma_f32_16x16x32_bf16 v[40:43], v[186:189], v[202:205], v[40:43]
	v_mfma_f32_16x16x32_bf16 v[32:35], v[194:197], v[202:205], v[32:35]
	v_mfma_f32_16x16x32_bf16 v[16:19], v[186:189], v[210:213], v[16:19]
	v_mfma_f32_16x16x32_bf16 v[8:11], v[194:197], v[210:213], v[8:11]
	v_mfma_f32_16x16x32_bf16 v[48:51], v[186:189], v[218:221], v[48:51]
	v_mfma_f32_16x16x32_bf16 v[52:55], v[194:197], v[218:221], v[52:55]
	v_mfma_f32_16x16x32_bf16 v[24:27], v[186:189], v[226:229], v[24:27]
	v_mfma_f32_16x16x32_bf16 v[28:31], v[194:197], v[226:229], v[28:31]
	s_setprio 0
	s_barrier
	s_add_i32 s67, 0, 0x18000
	v_add_u32_e32 v133, s67, v160
	s_add_i32 s68, 0, 0x1c000
	ds_read_b128 v[140:143], v133
	ds_read_b128 v[170:173], v133 offset:1024
	ds_read_b128 v[174:177], v133 offset:2048
	ds_read_b128 v[178:181], v133 offset:3072
	v_add_u32_e32 v133, s68, v160
	ds_read_b128 v[182:185], v133
	ds_read_b128 v[186:189], v133 offset:1024
	ds_read_b128 v[190:193], v133 offset:2048
	ds_read_b128 v[194:197], v133 offset:3072
	s_mov_b32 m0, s46
	ds_read_b128 v[198:201], v164 offset:32768
	ds_read_b128 v[202:205], v164 offset:33792
	ds_read_b128 v[206:209], v164 offset:34816
	ds_read_b128 v[210:213], v164 offset:35840
	ds_read_b128 v[214:217], v164 offset:36864
	ds_read_b128 v[218:221], v164 offset:37888
	ds_read_b128 v[222:225], v164 offset:38912
	ds_read_b128 v[226:229], v164 offset:39936
	global_load_lds_dwordx4 v129, s[42:43]
	s_mov_b32 m0, s47
	s_nop 0
	global_load_lds_dwordx4 v131, s[42:43]
	s_waitcnt vmcnt(8)
	s_waitcnt lgkmcnt(0)
	s_barrier
	s_setprio 1
	v_mfma_f32_16x16x32_bf16 v[124:127], v[140:143], v[198:201], v[124:127]
	v_mfma_f32_16x16x32_bf16 v[120:123], v[174:177], v[198:201], v[120:123]
	v_mfma_f32_16x16x32_bf16 v[116:119], v[140:143], v[206:209], v[116:119]
	v_mfma_f32_16x16x32_bf16 v[112:115], v[174:177], v[206:209], v[112:115]
	v_mfma_f32_16x16x32_bf16 v[108:111], v[140:143], v[214:217], v[108:111]
	v_mfma_f32_16x16x32_bf16 v[100:103], v[174:177], v[214:217], v[100:103]
	v_mfma_f32_16x16x32_bf16 v[92:95], v[140:143], v[222:225], v[92:95]
	v_mfma_f32_16x16x32_bf16 v[84:87], v[174:177], v[222:225], v[84:87]
	v_mfma_f32_16x16x32_bf16 v[124:127], v[170:173], v[202:205], v[124:127]
	v_mfma_f32_16x16x32_bf16 v[120:123], v[178:181], v[202:205], v[120:123]
	v_mfma_f32_16x16x32_bf16 v[116:119], v[170:173], v[210:213], v[116:119]
	v_mfma_f32_16x16x32_bf16 v[112:115], v[178:181], v[210:213], v[112:115]
	v_mfma_f32_16x16x32_bf16 v[108:111], v[170:173], v[218:221], v[108:111]
	v_mfma_f32_16x16x32_bf16 v[100:103], v[178:181], v[218:221], v[100:103]
	v_mfma_f32_16x16x32_bf16 v[92:95], v[170:173], v[226:229], v[92:95]
	v_mfma_f32_16x16x32_bf16 v[84:87], v[178:181], v[226:229], v[84:87]
	s_setprio 0
	s_setprio 1
	v_mfma_f32_16x16x32_bf16 v[104:107], v[182:185], v[198:201], v[104:107]
	v_mfma_f32_16x16x32_bf16 v[96:99], v[190:193], v[198:201], v[96:99]
	v_mfma_f32_16x16x32_bf16 v[88:91], v[182:185], v[206:209], v[88:91]
	v_mfma_f32_16x16x32_bf16 v[80:83], v[190:193], v[206:209], v[80:83]
	v_mfma_f32_16x16x32_bf16 v[76:79], v[182:185], v[214:217], v[76:79]
	v_mfma_f32_16x16x32_bf16 v[72:75], v[190:193], v[214:217], v[72:75]
	v_mfma_f32_16x16x32_bf16 v[68:71], v[182:185], v[222:225], v[68:71]
	v_mfma_f32_16x16x32_bf16 v[64:67], v[190:193], v[222:225], v[64:67]
	v_mfma_f32_16x16x32_bf16 v[104:107], v[186:189], v[202:205], v[104:107]
	v_mfma_f32_16x16x32_bf16 v[96:99], v[194:197], v[202:205], v[96:99]
	v_mfma_f32_16x16x32_bf16 v[88:91], v[186:189], v[210:213], v[88:91]
	v_mfma_f32_16x16x32_bf16 v[80:83], v[194:197], v[210:213], v[80:83]
	v_mfma_f32_16x16x32_bf16 v[76:79], v[186:189], v[218:221], v[76:79]
	v_mfma_f32_16x16x32_bf16 v[72:75], v[194:197], v[218:221], v[72:75]
	v_mfma_f32_16x16x32_bf16 v[68:71], v[186:189], v[226:229], v[68:71]
	v_mfma_f32_16x16x32_bf16 v[64:67], v[194:197], v[226:229], v[64:67]
	s_setprio 0
	s_barrier
	s_add_i32 s42, s67, s5
	v_lshl_add_u64 v[232:233], v[232:233], 0, s[20:21]
	s_mov_b32 m0, s42
	ds_read_b128 v[198:201], v164 offset:49152
	ds_read_b128 v[202:205], v164 offset:50176
	ds_read_b128 v[206:209], v164 offset:51200
	ds_read_b128 v[210:213], v164 offset:52224
	ds_read_b128 v[214:217], v164 offset:53248
	ds_read_b128 v[218:221], v164 offset:54272
	ds_read_b128 v[222:225], v164 offset:55296
	ds_read_b128 v[226:229], v164 offset:56320
	global_load_lds_dwordx4 v[232:233], off
	s_add_i32 m0, s42, 0x2000
	s_add_u32 s40, s40, 0x80080
	v_lshl_add_u64 v[232:233], v[234:235], 0, s[20:21]
	s_addc_u32 s41, s41, 0
	s_add_i32 s42, s68, s5
	global_load_lds_dwordx4 v[232:233], off
	v_lshl_add_u64 v[232:233], s[40:41], 0, v[146:147]
	s_mov_b32 m0, s42
	v_lshl_add_u64 v[230:231], v[230:231], 0, s[20:21]
	global_load_lds_dwordx4 v[232:233], off
	v_lshl_add_u64 v[232:233], s[40:41], 0, v[148:149]
	s_add_i32 m0, s42, 0x2000
	s_nop 0
	global_load_lds_dwordx4 v[232:233], off
	v_lshl_add_u64 v[232:233], v[236:237], 0, s[20:21]
	s_mov_b32 m0, s49
	s_nop 0
	global_load_lds_dwordx4 v[232:233], off
	s_mov_b32 m0, s51
	s_nop 0
	global_load_lds_dwordx4 v[230:231], off
	s_waitcnt vmcnt(8)
	s_waitcnt lgkmcnt(0)
	s_barrier
	s_setprio 1
	v_mfma_f32_16x16x32_bf16 v[60:63], v[140:143], v[198:201], v[60:63]
	v_mfma_f32_16x16x32_bf16 v[56:59], v[174:177], v[198:201], v[56:59]
	v_mfma_f32_16x16x32_bf16 v[44:47], v[140:143], v[206:209], v[44:47]
	v_mfma_f32_16x16x32_bf16 v[36:39], v[174:177], v[206:209], v[36:39]
	v_mfma_f32_16x16x32_bf16 v[20:23], v[140:143], v[214:217], v[20:23]
	v_mfma_f32_16x16x32_bf16 v[12:15], v[174:177], v[214:217], v[12:15]
	v_mfma_f32_16x16x32_bf16 v[4:7], v[140:143], v[222:225], v[4:7]
	v_mfma_f32_16x16x32_bf16 v[0:3], v[174:177], v[222:225], v[0:3]
	v_mfma_f32_16x16x32_bf16 v[60:63], v[170:173], v[202:205], v[60:63]
	v_mfma_f32_16x16x32_bf16 v[56:59], v[178:181], v[202:205], v[56:59]
	v_mfma_f32_16x16x32_bf16 v[44:47], v[170:173], v[210:213], v[44:47]
	v_mfma_f32_16x16x32_bf16 v[36:39], v[178:181], v[210:213], v[36:39]
	v_mfma_f32_16x16x32_bf16 v[20:23], v[170:173], v[218:221], v[20:23]
	v_mfma_f32_16x16x32_bf16 v[12:15], v[178:181], v[218:221], v[12:15]
	v_mfma_f32_16x16x32_bf16 v[4:7], v[170:173], v[226:229], v[4:7]
	v_mfma_f32_16x16x32_bf16 v[0:3], v[178:181], v[226:229], v[0:3]
	s_setprio 0
	s_setprio 1
	v_mfma_f32_16x16x32_bf16 v[40:43], v[182:185], v[198:201], v[40:43]
	v_mfma_f32_16x16x32_bf16 v[32:35], v[190:193], v[198:201], v[32:35]
	v_mfma_f32_16x16x32_bf16 v[16:19], v[182:185], v[206:209], v[16:19]
	v_mfma_f32_16x16x32_bf16 v[8:11], v[190:193], v[206:209], v[8:11]
	v_mfma_f32_16x16x32_bf16 v[48:51], v[182:185], v[214:217], v[48:51]
	v_mfma_f32_16x16x32_bf16 v[52:55], v[190:193], v[214:217], v[52:55]
	v_mfma_f32_16x16x32_bf16 v[24:27], v[182:185], v[222:225], v[24:27]
	v_mfma_f32_16x16x32_bf16 v[28:31], v[190:193], v[222:225], v[28:31]
	v_mfma_f32_16x16x32_bf16 v[40:43], v[186:189], v[202:205], v[40:43]
	v_mfma_f32_16x16x32_bf16 v[32:35], v[194:197], v[202:205], v[32:35]
	v_mfma_f32_16x16x32_bf16 v[16:19], v[186:189], v[210:213], v[16:19]
	v_mfma_f32_16x16x32_bf16 v[8:11], v[194:197], v[210:213], v[8:11]
	v_mfma_f32_16x16x32_bf16 v[48:51], v[186:189], v[218:221], v[48:51]
	v_mfma_f32_16x16x32_bf16 v[52:55], v[194:197], v[218:221], v[52:55]
	v_mfma_f32_16x16x32_bf16 v[24:27], v[186:189], v[226:229], v[24:27]
	v_mfma_f32_16x16x32_bf16 v[28:31], v[194:197], v[226:229], v[28:31]
	s_setprio 0
	s_add_i32 s66, s66, 2
	s_add_u32 s8, s8, 0x100
	s_addc_u32 s9, s9, 0
	s_cmp_gt_u32 s66, 29
	s_barrier
	s_cbranch_scc0 .LBB0_2355
	s_and_b64 vcc, exec, s[22:23]
	s_cbranch_vccz .LBB0_2358
	s_barrier

.LBB0_2750:
	v_add_u32_e32 v163, s48, v143
	ds_read_b128 v[164:167], v163
	ds_read_b128 v[168:171], v163 offset:1024
	ds_read_b128 v[172:175], v163 offset:2048
	ds_read_b128 v[176:179], v163 offset:3072
	v_add_u32_e32 v163, s49, v143
	ds_read_b128 v[180:183], v163
	ds_read_b128 v[184:187], v163 offset:1024
	ds_read_b128 v[188:191], v163 offset:2048
	ds_read_b128 v[192:195], v163 offset:3072
	s_cmpk_eq_i32 s8, 0x1000
	s_cselect_b64 vcc, -1, 0
	s_and_b64 s[40:41], vcc, exec
	s_cselect_b32 s40, 0, s8
	v_lshl_add_u64 v[196:197], v[148:149], 0, s[8:9]
	s_cselect_b32 s41, 0, s9
	s_add_u32 s40, s18, s40
	v_cndmask_b32_e32 v132, v146, v158, vcc
	v_cndmask_b32_e32 v139, v140, v160, vcc
	v_cndmask_b32_e32 v228, v142, v159, vcc
	v_cndmask_b32_e32 v141, v138, v161, vcc
	v_cndmask_b32_e32 v230, v196, v162, vcc
	v_cndmask_b32_e32 v231, v197, v135, vcc
	s_addc_u32 s41, s19, s41
	v_lshl_add_u64 v[232:233], v[152:153], 0, s[8:9]
	s_mov_b32 m0, s52
	v_lshl_add_u64 v[232:233], v[232:233], 0, s[36:37]
	ds_read_b128 v[196:199], v157
	ds_read_b128 v[200:203], v157 offset:1024
	ds_read_b128 v[204:207], v157 offset:2048
	ds_read_b128 v[208:211], v157 offset:3072
	ds_read_b128 v[212:215], v157 offset:4096
	ds_read_b128 v[216:219], v157 offset:5120
	ds_read_b128 v[220:223], v157 offset:6144
	ds_read_b128 v[224:227], v157 offset:7168
	global_load_lds_dwordx4 v[232:233], off
	v_lshl_add_u64 v[232:233], v[150:151], 0, s[8:9]
	v_lshl_add_u64 v[232:233], v[232:233], 0, s[36:37]
	s_mov_b32 m0, s53
	s_nop 0
	global_load_lds_dwordx4 v[232:233], off
	s_waitcnt vmcnt(8)
	s_waitcnt lgkmcnt(0)
	s_barrier
	s_setprio 1
	v_mfma_f32_16x16x32_bf16 v[124:127], v[164:167], v[196:199], v[124:127]
	v_mfma_f32_16x16x32_bf16 v[120:123], v[172:175], v[196:199], v[120:123]
	v_mfma_f32_16x16x32_bf16 v[108:111], v[164:167], v[204:207], v[108:111]
	v_mfma_f32_16x16x32_bf16 v[104:107], v[172:175], v[204:207], v[104:107]
	v_mfma_f32_16x16x32_bf16 v[92:95], v[164:167], v[212:215], v[92:95]
	v_mfma_f32_16x16x32_bf16 v[88:91], v[172:175], v[212:215], v[88:91]
	v_mfma_f32_16x16x32_bf16 v[76:79], v[164:167], v[220:223], v[76:79]
	v_mfma_f32_16x16x32_bf16 v[72:75], v[172:175], v[220:223], v[72:75]
	v_mfma_f32_16x16x32_bf16 v[124:127], v[168:171], v[200:203], v[124:127]
	v_mfma_f32_16x16x32_bf16 v[120:123], v[176:179], v[200:203], v[120:123]
	v_mfma_f32_16x16x32_bf16 v[108:111], v[168:171], v[208:211], v[108:111]
	v_mfma_f32_16x16x32_bf16 v[104:107], v[176:179], v[208:211], v[104:107]
	v_mfma_f32_16x16x32_bf16 v[92:95], v[168:171], v[216:219], v[92:95]
	v_mfma_f32_16x16x32_bf16 v[88:91], v[176:179], v[216:219], v[88:91]
	v_mfma_f32_16x16x32_bf16 v[76:79], v[168:171], v[224:227], v[76:79]
	v_mfma_f32_16x16x32_bf16 v[72:75], v[176:179], v[224:227], v[72:75]
	s_setprio 0
	s_setprio 1
	v_mfma_f32_16x16x32_bf16 v[116:119], v[180:183], v[196:199], v[116:119]
	v_mfma_f32_16x16x32_bf16 v[112:115], v[188:191], v[196:199], v[112:115]
	v_mfma_f32_16x16x32_bf16 v[100:103], v[180:183], v[204:207], v[100:103]
	v_mfma_f32_16x16x32_bf16 v[96:99], v[188:191], v[204:207], v[96:99]
	v_mfma_f32_16x16x32_bf16 v[84:87], v[180:183], v[212:215], v[84:87]
	v_mfma_f32_16x16x32_bf16 v[80:83], v[188:191], v[212:215], v[80:83]
	v_mfma_f32_16x16x32_bf16 v[68:71], v[180:183], v[220:223], v[68:71]
	v_mfma_f32_16x16x32_bf16 v[64:67], v[188:191], v[220:223], v[64:67]
	v_mfma_f32_16x16x32_bf16 v[116:119], v[184:187], v[200:203], v[116:119]
	v_mfma_f32_16x16x32_bf16 v[112:115], v[192:195], v[200:203], v[112:115]
	v_mfma_f32_16x16x32_bf16 v[100:103], v[184:187], v[208:211], v[100:103]
	v_mfma_f32_16x16x32_bf16 v[96:99], v[192:195], v[208:211], v[96:99]
	v_mfma_f32_16x16x32_bf16 v[84:87], v[184:187], v[216:219], v[84:87]
	v_mfma_f32_16x16x32_bf16 v[80:83], v[192:195], v[216:219], v[80:83]
	v_mfma_f32_16x16x32_bf16 v[68:71], v[184:187], v[224:227], v[68:71]
	v_mfma_f32_16x16x32_bf16 v[64:67], v[192:195], v[224:227], v[64:67]
	s_setprio 0
	s_barrier
	s_mov_b32 m0, s55
	v_lshl_add_u64 v[232:233], v[230:231], 0, v[128:129]
	ds_read_b128 v[196:199], v157 offset:16384
	ds_read_b128 v[200:203], v157 offset:17408
	ds_read_b128 v[204:207], v157 offset:18432
	ds_read_b128 v[208:211], v157 offset:19456
	ds_read_b128 v[212:215], v157 offset:20480
	ds_read_b128 v[216:219], v157 offset:21504
	ds_read_b128 v[220:223], v157 offset:22528
	ds_read_b128 v[224:227], v157 offset:23552
	global_load_lds_dwordx4 v[232:233], off
	v_lshl_add_u64 v[234:235], v[230:231], 0, v[130:131]
	s_mov_b32 m0, s57
	v_lshl_add_u64 v[236:237], v[230:231], 0, s[24:25]
	global_load_lds_dwordx4 v[234:235], off
	v_lshl_add_u64 v[238:239], v[236:237], 0, v[128:129]
	s_mov_b32 m0, s59
	v_lshl_add_u64 v[236:237], v[236:237], 0, v[130:131]
	global_load_lds_dwordx4 v[238:239], off
	s_mov_b32 m0, s60
	v_mov_b32_e32 v229, v133
	global_load_lds_dwordx4 v[236:237], off
	s_mov_b32 m0, s1
	v_lshl_add_u64 v[236:237], s[40:41], 0, v[132:133]
	global_load_lds_dwordx4 v132, s[40:41]
	s_mov_b32 m0, s22
	s_nop 0
	global_load_lds_dwordx4 v228, s[40:41]
	s_waitcnt vmcnt(8)
	s_waitcnt lgkmcnt(0)
	v_lshl_add_u64 v[228:229], s[40:41], 0, v[228:229]
	s_barrier
	s_setprio 1
	v_mfma_f32_16x16x32_bf16 v[60:63], v[164:167], v[196:199], v[60:63]
	v_mfma_f32_16x16x32_bf16 v[56:59], v[172:175], v[196:199], v[56:59]
	v_mfma_f32_16x16x32_bf16 v[44:47], v[164:167], v[204:207], v[44:47]
	v_mfma_f32_16x16x32_bf16 v[36:39], v[172:175], v[204:207], v[36:39]
	v_mfma_f32_16x16x32_bf16 v[20:23], v[164:167], v[212:215], v[20:23]
	v_mfma_f32_16x16x32_bf16 v[8:11], v[172:175], v[212:215], v[8:11]
	v_mfma_f32_16x16x32_bf16 v[4:7], v[164:167], v[220:223], v[4:7]
	v_mfma_f32_16x16x32_bf16 v[0:3], v[172:175], v[220:223], v[0:3]
	v_mfma_f32_16x16x32_bf16 v[60:63], v[168:171], v[200:203], v[60:63]
	v_mfma_f32_16x16x32_bf16 v[56:59], v[176:179], v[200:203], v[56:59]
	v_mfma_f32_16x16x32_bf16 v[44:47], v[168:171], v[208:211], v[44:47]
	v_mfma_f32_16x16x32_bf16 v[36:39], v[176:179], v[208:211], v[36:39]
	v_mfma_f32_16x16x32_bf16 v[20:23], v[168:171], v[216:219], v[20:23]
	v_mfma_f32_16x16x32_bf16 v[8:11], v[176:179], v[216:219], v[8:11]
	v_mfma_f32_16x16x32_bf16 v[4:7], v[168:171], v[224:227], v[4:7]
	v_mfma_f32_16x16x32_bf16 v[0:3], v[176:179], v[224:227], v[0:3]
	s_setprio 0
	s_setprio 1
	v_mfma_f32_16x16x32_bf16 v[52:55], v[180:183], v[196:199], v[52:55]
	v_mfma_f32_16x16x32_bf16 v[48:51], v[188:191], v[196:199], v[48:51]
	v_mfma_f32_16x16x32_bf16 v[28:31], v[180:183], v[204:207], v[28:31]
	v_mfma_f32_16x16x32_bf16 v[24:27], v[188:191], v[204:207], v[24:27]
	v_mfma_f32_16x16x32_bf16 v[40:43], v[180:183], v[212:215], v[40:43]
	v_mfma_f32_16x16x32_bf16 v[32:35], v[188:191], v[212:215], v[32:35]
	v_mfma_f32_16x16x32_bf16 v[16:19], v[180:183], v[220:223], v[16:19]
	v_mfma_f32_16x16x32_bf16 v[12:15], v[188:191], v[220:223], v[12:15]
	v_mfma_f32_16x16x32_bf16 v[52:55], v[184:187], v[200:203], v[52:55]
	v_mfma_f32_16x16x32_bf16 v[48:51], v[192:195], v[200:203], v[48:51]
	v_mfma_f32_16x16x32_bf16 v[28:31], v[184:187], v[208:211], v[28:31]
	v_mfma_f32_16x16x32_bf16 v[24:27], v[192:195], v[208:211], v[24:27]
	v_mfma_f32_16x16x32_bf16 v[40:43], v[184:187], v[216:219], v[40:43]
	v_mfma_f32_16x16x32_bf16 v[32:35], v[192:195], v[216:219], v[32:35]
	v_mfma_f32_16x16x32_bf16 v[16:19], v[184:187], v[224:227], v[16:19]
	v_mfma_f32_16x16x32_bf16 v[12:15], v[192:195], v[224:227], v[12:15]
	s_setprio 0
	s_barrier
	v_add_u32_e32 v132, s61, v143
	s_add_i32 s51, 0, 0x1c000
	ds_read_b128 v[164:167], v132
	ds_read_b128 v[168:171], v132 offset:1024
	ds_read_b128 v[172:175], v132 offset:2048
	ds_read_b128 v[176:179], v132 offset:3072
	v_add_u32_e32 v132, s51, v143
	ds_read_b128 v[180:183], v132
	ds_read_b128 v[184:187], v132 offset:1024
	ds_read_b128 v[188:191], v132 offset:2048
	ds_read_b128 v[192:195], v132 offset:3072
	s_mov_b32 m0, s42
	ds_read_b128 v[196:199], v157 offset:32768
	ds_read_b128 v[200:203], v157 offset:33792
	ds_read_b128 v[204:207], v157 offset:34816
	ds_read_b128 v[208:211], v157 offset:35840
	ds_read_b128 v[212:215], v157 offset:36864
	ds_read_b128 v[216:219], v157 offset:37888
	ds_read_b128 v[220:223], v157 offset:38912
	ds_read_b128 v[224:227], v157 offset:39936
	global_load_lds_dwordx4 v139, s[40:41]
	s_mov_b32 m0, s43
	s_nop 0
	global_load_lds_dwordx4 v141, s[40:41]
	s_waitcnt vmcnt(8)
	s_waitcnt lgkmcnt(0)
	s_barrier
	s_setprio 1
	v_mfma_f32_16x16x32_bf16 v[124:127], v[164:167], v[196:199], v[124:127]
	v_mfma_f32_16x16x32_bf16 v[120:123], v[172:175], v[196:199], v[120:123]
	v_mfma_f32_16x16x32_bf16 v[108:111], v[164:167], v[204:207], v[108:111]
	v_mfma_f32_16x16x32_bf16 v[104:107], v[172:175], v[204:207], v[104:107]
	v_mfma_f32_16x16x32_bf16 v[92:95], v[164:167], v[212:215], v[92:95]
	v_mfma_f32_16x16x32_bf16 v[88:91], v[172:175], v[212:215], v[88:91]
	v_mfma_f32_16x16x32_bf16 v[76:79], v[164:167], v[220:223], v[76:79]
	v_mfma_f32_16x16x32_bf16 v[72:75], v[172:175], v[220:223], v[72:75]
	v_mfma_f32_16x16x32_bf16 v[124:127], v[168:171], v[200:203], v[124:127]
	v_mfma_f32_16x16x32_bf16 v[120:123], v[176:179], v[200:203], v[120:123]
	v_mfma_f32_16x16x32_bf16 v[108:111], v[168:171], v[208:211], v[108:111]
	v_mfma_f32_16x16x32_bf16 v[104:107], v[176:179], v[208:211], v[104:107]
	v_mfma_f32_16x16x32_bf16 v[92:95], v[168:171], v[216:219], v[92:95]
	v_mfma_f32_16x16x32_bf16 v[88:91], v[176:179], v[216:219], v[88:91]
	v_mfma_f32_16x16x32_bf16 v[76:79], v[168:171], v[224:227], v[76:79]
	v_mfma_f32_16x16x32_bf16 v[72:75], v[176:179], v[224:227], v[72:75]
	s_setprio 0
	s_setprio 1
	v_mfma_f32_16x16x32_bf16 v[116:119], v[180:183], v[196:199], v[116:119]
	v_mfma_f32_16x16x32_bf16 v[112:115], v[188:191], v[196:199], v[112:115]
	v_mfma_f32_16x16x32_bf16 v[100:103], v[180:183], v[204:207], v[100:103]
	v_mfma_f32_16x16x32_bf16 v[96:99], v[188:191], v[204:207], v[96:99]
	v_mfma_f32_16x16x32_bf16 v[84:87], v[180:183], v[212:215], v[84:87]
	v_mfma_f32_16x16x32_bf16 v[80:83], v[188:191], v[212:215], v[80:83]
	v_mfma_f32_16x16x32_bf16 v[68:71], v[180:183], v[220:223], v[68:71]
	v_mfma_f32_16x16x32_bf16 v[64:67], v[188:191], v[220:223], v[64:67]
	v_mfma_f32_16x16x32_bf16 v[116:119], v[184:187], v[200:203], v[116:119]
	v_mfma_f32_16x16x32_bf16 v[112:115], v[192:195], v[200:203], v[112:115]
	v_mfma_f32_16x16x32_bf16 v[100:103], v[184:187], v[208:211], v[100:103]
	v_mfma_f32_16x16x32_bf16 v[96:99], v[192:195], v[208:211], v[96:99]
	v_mfma_f32_16x16x32_bf16 v[84:87], v[184:187], v[216:219], v[84:87]
	v_mfma_f32_16x16x32_bf16 v[80:83], v[192:195], v[216:219], v[80:83]
	v_mfma_f32_16x16x32_bf16 v[68:71], v[184:187], v[224:227], v[68:71]
	v_mfma_f32_16x16x32_bf16 v[64:67], v[192:195], v[224:227], v[64:67]
	s_setprio 0
	s_barrier
	s_add_i32 s40, s61, s0
	v_lshl_add_u64 v[232:233], v[232:233], 0, s[28:29]
	s_mov_b32 m0, s40
	ds_read_b128 v[196:199], v157 offset:49152
	ds_read_b128 v[200:203], v157 offset:50176
	ds_read_b128 v[204:207], v157 offset:51200
	ds_read_b128 v[208:211], v157 offset:52224
	ds_read_b128 v[212:215], v157 offset:53248
	ds_read_b128 v[216:219], v157 offset:54272
	ds_read_b128 v[220:223], v157 offset:55296
	ds_read_b128 v[224:227], v157 offset:56320
	global_load_lds_dwordx4 v[232:233], off
	v_lshl_add_u64 v[232:233], v[234:235], 0, s[28:29]
	s_add_i32 m0, s40, 0x2000
	v_lshl_add_u64 v[230:231], v[230:231], 0, s[30:31]
	s_add_i32 s40, s51, s0
	global_load_lds_dwordx4 v[232:233], off
	v_lshl_add_u64 v[232:233], v[230:231], 0, v[128:129]
	s_mov_b32 m0, s40
	v_lshl_add_u64 v[230:231], v[230:231], 0, v[130:131]
	global_load_lds_dwordx4 v[232:233], off
	s_add_i32 m0, s40, 0x2000
	v_lshl_add_u64 v[228:229], v[228:229], 0, s[28:29]
	global_load_lds_dwordx4 v[230:231], off
	v_lshl_add_u64 v[230:231], v[236:237], 0, s[28:29]
	s_mov_b32 m0, s46
	s_nop 0
	global_load_lds_dwordx4 v[230:231], off
	s_mov_b32 m0, s47
	s_nop 0
	global_load_lds_dwordx4 v[228:229], off
	s_waitcnt vmcnt(8)
	s_waitcnt lgkmcnt(0)
	s_barrier
	s_setprio 1
	v_mfma_f32_16x16x32_bf16 v[60:63], v[164:167], v[196:199], v[60:63]
	v_mfma_f32_16x16x32_bf16 v[56:59], v[172:175], v[196:199], v[56:59]
	v_mfma_f32_16x16x32_bf16 v[44:47], v[164:167], v[204:207], v[44:47]
	v_mfma_f32_16x16x32_bf16 v[36:39], v[172:175], v[204:207], v[36:39]
	v_mfma_f32_16x16x32_bf16 v[20:23], v[164:167], v[212:215], v[20:23]
	v_mfma_f32_16x16x32_bf16 v[8:11], v[172:175], v[212:215], v[8:11]
	v_mfma_f32_16x16x32_bf16 v[4:7], v[164:167], v[220:223], v[4:7]
	v_mfma_f32_16x16x32_bf16 v[0:3], v[172:175], v[220:223], v[0:3]
	v_mfma_f32_16x16x32_bf16 v[60:63], v[168:171], v[200:203], v[60:63]
	v_mfma_f32_16x16x32_bf16 v[56:59], v[176:179], v[200:203], v[56:59]
	v_mfma_f32_16x16x32_bf16 v[44:47], v[168:171], v[208:211], v[44:47]
	v_mfma_f32_16x16x32_bf16 v[36:39], v[176:179], v[208:211], v[36:39]
	v_mfma_f32_16x16x32_bf16 v[20:23], v[168:171], v[216:219], v[20:23]
	v_mfma_f32_16x16x32_bf16 v[8:11], v[176:179], v[216:219], v[8:11]
	v_mfma_f32_16x16x32_bf16 v[4:7], v[168:171], v[224:227], v[4:7]
	v_mfma_f32_16x16x32_bf16 v[0:3], v[176:179], v[224:227], v[0:3]
	s_setprio 0
	s_setprio 1
	v_mfma_f32_16x16x32_bf16 v[52:55], v[180:183], v[196:199], v[52:55]
	v_mfma_f32_16x16x32_bf16 v[48:51], v[188:191], v[196:199], v[48:51]
	v_mfma_f32_16x16x32_bf16 v[28:31], v[180:183], v[204:207], v[28:31]
	v_mfma_f32_16x16x32_bf16 v[24:27], v[188:191], v[204:207], v[24:27]
	v_mfma_f32_16x16x32_bf16 v[40:43], v[180:183], v[212:215], v[40:43]
	v_mfma_f32_16x16x32_bf16 v[32:35], v[188:191], v[212:215], v[32:35]
	v_mfma_f32_16x16x32_bf16 v[16:19], v[180:183], v[220:223], v[16:19]
	v_mfma_f32_16x16x32_bf16 v[12:15], v[188:191], v[220:223], v[12:15]
	v_mfma_f32_16x16x32_bf16 v[52:55], v[184:187], v[200:203], v[52:55]
	v_mfma_f32_16x16x32_bf16 v[48:51], v[192:195], v[200:203], v[48:51]
	v_mfma_f32_16x16x32_bf16 v[28:31], v[184:187], v[208:211], v[28:31]
	v_mfma_f32_16x16x32_bf16 v[24:27], v[192:195], v[208:211], v[24:27]
	v_mfma_f32_16x16x32_bf16 v[40:43], v[184:187], v[216:219], v[40:43]
	v_mfma_f32_16x16x32_bf16 v[32:35], v[192:195], v[216:219], v[32:35]
	v_mfma_f32_16x16x32_bf16 v[16:19], v[184:187], v[224:227], v[16:19]
	v_mfma_f32_16x16x32_bf16 v[12:15], v[192:195], v[224:227], v[12:15]
	s_setprio 0
	s_add_i32 s39, s39, 2
	s_add_u32 s8, s8, 0x100
	s_addc_u32 s9, s9, 0
	s_cmp_gt_u32 s39, 29
	s_barrier
	s_cbranch_scc0 .LBB0_2750
	s_and_b64 vcc, exec, s[34:35]
	s_cbranch_vccz .LBB0_2753
	s_barrier
